# expert-weight conversion fp8 stores nt (on top of P1 nt)
# speedup vs baseline: 1.0050x; 1.0050x over previous
.LBB0_465:
	s_or_b64 exec, exec, s[4:5]
	s_waitcnt lgkmcnt(0)
	s_barrier
	ds_read_b32 v4, v12
	s_mov_b64 s[4:5], -1
	s_waitcnt lgkmcnt(0)
	v_cmp_lt_u32_e32 vcc, s16, v4
	v_readfirstlane_b32 s2, v4
	s_cbranch_vccnz .LBB0_458
	s_lshl_b32 s6, s2, 3
	s_add_i32 s6, s6, s91
	s_cmpk_gt_u32 s6, 0x5fff
	s_cbranch_scc1 .LBB0_457
	s_lshl_b32 s7, s6, 5
	s_cmpk_gt_u32 s6, 0x3fff
	s_cbranch_scc0 .LBB0_469
	s_add_i32 s2, s6, 0xffffc000
	s_lshr_b32 s2, s2, 8
	s_lshl_b64 s[4:5], s[2:3], 20
	s_lshl_b64 s[8:9], s[2:3], 22
	s_add_u32 s8, s76, s8
	s_addc_u32 s9, s77, s9
	s_add_u32 s4, s10, s4
	s_addc_u32 s5, s11, s5
	s_lshl_b32 s2, s6, 2
	s_and_b32 s44, s2, 0x380
	s_and_b32 s2, s7, 0x3e0
	v_or_b32_e32 v4, s2, v6
	v_or_b32_e32 v42, s44, v7
	v_lshlrev_b32_e32 v4, 2, v4
	v_lshl_add_u64 v[40:41], s[8:9], 0, v[4:5]
	v_lshlrev_b32_e32 v4, 12, v42
	v_lshl_add_u64 v[96:97], v[40:41], 0, v[4:5]
	v_add_co_u32_e32 v44, vcc, s17, v96
	global_load_dwordx4 v[40:43], v[96:97], off nt
	s_nop 0
	v_addc_co_u32_e32 v45, vcc, 0, v97, vcc
	global_load_dwordx4 v[44:47], v[44:45], off nt
	v_add_co_u32_e32 v48, vcc, s18, v96
	s_add_u32 s4, s4, s44
	s_nop 0
	v_addc_co_u32_e32 v49, vcc, 0, v97, vcc
	v_add_co_u32_e32 v52, vcc, s19, v96
	global_load_dwordx4 v[48:51], v[48:49], off nt
	s_nop 0
	v_addc_co_u32_e32 v53, vcc, 0, v97, vcc
	global_load_dwordx4 v[52:55], v[52:53], off nt
	v_add_co_u32_e32 v56, vcc, s20, v96
	s_addc_u32 s5, s5, 0
	s_nop 0
	v_addc_co_u32_e32 v57, vcc, 0, v97, vcc
	v_add_co_u32_e32 v60, vcc, s21, v96
	global_load_dwordx4 v[56:59], v[56:57], off nt
	s_nop 0
	v_addc_co_u32_e32 v61, vcc, 0, v97, vcc
	global_load_dwordx4 v[60:63], v[60:61], off nt
	v_add_co_u32_e32 v64, vcc, s22, v96
	s_nop 1
	v_addc_co_u32_e32 v65, vcc, 0, v97, vcc
	v_add_co_u32_e32 v68, vcc, s23, v96
	global_load_dwordx4 v[64:67], v[64:65], off nt
	s_nop 0
	v_addc_co_u32_e32 v69, vcc, 0, v97, vcc
	global_load_dwordx4 v[68:71], v[68:69], off nt
	v_add_co_u32_e32 v72, vcc, s24, v96
	s_waitcnt vmcnt(7)
	v_mul_f32_e32 v4, 0x42800000, v40
	v_addc_co_u32_e32 v73, vcc, 0, v97, vcc
	v_add_co_u32_e32 v76, vcc, s25, v96
	v_mul_f32_e32 v40, 0x42800000, v41
	s_nop 0
	v_addc_co_u32_e32 v77, vcc, 0, v97, vcc
	global_load_dwordx4 v[72:75], v[72:73], off nt
	s_nop 0
	global_load_dwordx4 v[76:79], v[76:77], off nt
	v_add_co_u32_e32 v80, vcc, s26, v96
	v_mul_f32_e32 v41, 0x42800000, v42
	s_nop 0
	v_addc_co_u32_e32 v81, vcc, 0, v97, vcc
	v_add_co_u32_e32 v84, vcc, s27, v96
	v_mul_f32_e32 v42, 0x42800000, v43
	s_nop 0
	v_addc_co_u32_e32 v85, vcc, 0, v97, vcc
	global_load_dwordx4 v[80:83], v[80:81], off nt
	s_nop 0
	global_load_dwordx4 v[84:87], v[84:85], off nt
	v_add_co_u32_e32 v88, vcc, s28, v96
	s_waitcnt vmcnt(10)
	v_mul_f32_e32 v43, 0x42800000, v44
	v_addc_co_u32_e32 v89, vcc, 0, v97, vcc
	v_add_co_u32_e32 v92, vcc, s29, v96
	s_nop 1
	v_addc_co_u32_e32 v93, vcc, 0, v97, vcc
	global_load_dwordx4 v[88:91], v[88:89], off nt
	s_nop 0
	global_load_dwordx4 v[92:95], v[92:93], off nt
	v_add_co_u32_e32 v98, vcc, s30, v96
	s_nop 1
	v_addc_co_u32_e32 v99, vcc, 0, v97, vcc
	v_add_co_u32_e32 v100, vcc, s31, v96
	s_nop 1
	v_addc_co_u32_e32 v101, vcc, 0, v97, vcc
	global_load_dwordx4 v[96:99], v[98:99], off nt
	s_nop 0
	global_load_dwordx4 v[100:103], v[100:101], off nt
	ds_write2_b32 v8, v4, v43 offset1:8
	v_mul_f32_e32 v4, 0x42800000, v45
	ds_write2_b32 v8, v40, v4 offset0:129 offset1:137
	v_mul_f32_e32 v4, 0x42800000, v46
	ds_write2_b32 v38, v41, v4 offset0:2 offset1:10
	v_mul_f32_e32 v4, 0x42800000, v47
	ds_write2_b32 v38, v42, v4 offset0:131 offset1:139
	s_waitcnt vmcnt(13)
	v_mul_f32_e32 v4, 0x42800000, v48
	s_waitcnt vmcnt(12)
	v_mul_f32_e32 v43, 0x42800000, v52
	v_mul_f32_e32 v40, 0x42800000, v49
	ds_write2_b32 v8, v4, v43 offset0:16 offset1:24
	v_mul_f32_e32 v4, 0x42800000, v53
	v_mul_f32_e32 v41, 0x42800000, v50
	ds_write2_b32 v8, v40, v4 offset0:145 offset1:153
	v_mul_f32_e32 v4, 0x42800000, v54
	v_mul_f32_e32 v42, 0x42800000, v51
	ds_write2_b32 v38, v41, v4 offset0:18 offset1:26
	v_mul_f32_e32 v4, 0x42800000, v55
	ds_write2_b32 v38, v42, v4 offset0:147 offset1:155
	s_waitcnt vmcnt(11)
	v_mul_f32_e32 v4, 0x42800000, v56
	s_waitcnt vmcnt(10)
	v_mul_f32_e32 v43, 0x42800000, v60
	v_mul_f32_e32 v40, 0x42800000, v57
	ds_write2_b32 v8, v4, v43 offset0:32 offset1:40
	v_mul_f32_e32 v4, 0x42800000, v61
	v_mul_f32_e32 v41, 0x42800000, v58
	ds_write2_b32 v8, v40, v4 offset0:161 offset1:169
	v_mul_f32_e32 v4, 0x42800000, v62
	v_mul_f32_e32 v42, 0x42800000, v59
	ds_write2_b32 v38, v41, v4 offset0:34 offset1:42
	v_mul_f32_e32 v4, 0x42800000, v63
	ds_write2_b32 v38, v42, v4 offset0:163 offset1:171
	s_waitcnt vmcnt(9)
	v_mul_f32_e32 v4, 0x42800000, v64
	s_waitcnt vmcnt(8)
	v_mul_f32_e32 v43, 0x42800000, v68
	v_mul_f32_e32 v40, 0x42800000, v65
	ds_write2_b32 v8, v4, v43 offset0:48 offset1:56
	v_mul_f32_e32 v4, 0x42800000, v69
	v_mul_f32_e32 v41, 0x42800000, v66
	ds_write2_b32 v8, v40, v4 offset0:177 offset1:185
	v_mul_f32_e32 v4, 0x42800000, v70
	v_mul_f32_e32 v42, 0x42800000, v67
	ds_write2_b32 v38, v41, v4 offset0:50 offset1:58
	v_mul_f32_e32 v4, 0x42800000, v71
	ds_write2_b32 v38, v42, v4 offset0:179 offset1:187
	v_lshl_add_u64 v[48:49], s[4:5], 0, v[2:3]
	s_mov_b64 s[4:5], 0
	s_waitcnt vmcnt(7)
	v_mul_f32_e32 v4, 0x42800000, v72
	s_waitcnt vmcnt(6)
	v_mul_f32_e32 v43, 0x42800000, v76
	v_mul_f32_e32 v40, 0x42800000, v73
	ds_write2_b32 v8, v4, v43 offset0:64 offset1:72
	v_mul_f32_e32 v4, 0x42800000, v77
	v_mul_f32_e32 v41, 0x42800000, v74
	ds_write2_b32 v8, v40, v4 offset0:193 offset1:201
	v_mul_f32_e32 v4, 0x42800000, v78
	v_mul_f32_e32 v42, 0x42800000, v75
	ds_write2_b32 v38, v41, v4 offset0:66 offset1:74
	v_mul_f32_e32 v4, 0x42800000, v79
	ds_write2_b32 v38, v42, v4 offset0:195 offset1:203
	s_waitcnt vmcnt(5)
	v_mul_f32_e32 v4, 0x42800000, v80
	s_waitcnt vmcnt(4)
	v_mul_f32_e32 v43, 0x42800000, v84
	v_mul_f32_e32 v40, 0x42800000, v81
	ds_write2_b32 v8, v4, v43 offset0:80 offset1:88
	v_mul_f32_e32 v4, 0x42800000, v85
	v_mul_f32_e32 v41, 0x42800000, v82
	ds_write2_b32 v8, v40, v4 offset0:209 offset1:217
	v_mul_f32_e32 v4, 0x42800000, v86
	v_mul_f32_e32 v42, 0x42800000, v83
	ds_write2_b32 v38, v41, v4 offset0:82 offset1:90
	v_mul_f32_e32 v4, 0x42800000, v87
	ds_write2_b32 v38, v42, v4 offset0:211 offset1:219
	s_waitcnt vmcnt(3)
	v_mul_f32_e32 v4, 0x42800000, v88
	s_waitcnt vmcnt(2)
	v_mul_f32_e32 v43, 0x42800000, v92
	v_mul_f32_e32 v40, 0x42800000, v89
	ds_write2_b32 v8, v4, v43 offset0:96 offset1:104
	v_mul_f32_e32 v4, 0x42800000, v93
	v_mul_f32_e32 v41, 0x42800000, v90
	ds_write2_b32 v8, v40, v4 offset0:225 offset1:233
	v_mul_f32_e32 v4, 0x42800000, v94
	v_mul_f32_e32 v42, 0x42800000, v91
	ds_write2_b32 v38, v41, v4 offset0:98 offset1:106
	v_mul_f32_e32 v4, 0x42800000, v95
	ds_write2_b32 v38, v42, v4 offset0:227 offset1:235
	s_waitcnt vmcnt(1)
	v_mul_f32_e32 v4, 0x42800000, v96
	s_waitcnt vmcnt(0)
	v_mul_f32_e32 v43, 0x42800000, v100
	v_mul_f32_e32 v40, 0x42800000, v97
	ds_write2_b32 v8, v4, v43 offset0:112 offset1:120
	v_mul_f32_e32 v4, 0x42800000, v101
	v_mul_f32_e32 v41, 0x42800000, v98
	ds_write2_b32 v8, v40, v4 offset0:241 offset1:249
	v_mul_f32_e32 v4, 0x42800000, v102
	v_mul_f32_e32 v42, 0x42800000, v99
	ds_write2_b32 v38, v41, v4 offset0:114 offset1:122
	v_mul_f32_e32 v4, 0x42800000, v103
	ds_write2_b32 v38, v42, v4 offset0:243 offset1:251
	s_waitcnt lgkmcnt(0)
	ds_read2_b32 v[40:41], v13 offset1:1
	ds_read2_b32 v[42:43], v13 offset0:2 offset1:3
	ds_read2_b32 v[44:45], v13 offset0:4 offset1:5
	ds_read2_b32 v[46:47], v13 offset0:6 offset1:7
	s_waitcnt lgkmcnt(3)
	v_med3_f32 v4, v40, s33, v39
	v_med3_f32 v41, v41, s33, v39
	v_mov_b32_e32 v40, v5
	v_cvt_pk_fp8_f32 v40, v4, v41
	s_waitcnt lgkmcnt(2)
	v_med3_f32 v4, v42, s33, v39
	v_med3_f32 v41, v43, s33, v39
	s_waitcnt lgkmcnt(1)
	v_med3_f32 v42, v45, s33, v39
	v_cvt_pk_fp8_f32 v40, v4, v41 op_sel:[0,0,1]
	v_med3_f32 v4, v44, s33, v39
	v_mov_b32_e32 v41, v5
	v_cvt_pk_fp8_f32 v41, v4, v42
	ds_read2_b32 v[42:43], v13 offset0:8 offset1:9
	s_waitcnt lgkmcnt(1)
	v_med3_f32 v4, v46, s33, v39
	v_med3_f32 v44, v47, s33, v39
	v_cvt_pk_fp8_f32 v41, v4, v44 op_sel:[0,0,1]
	ds_read2_b32 v[44:45], v13 offset0:10 offset1:11
	ds_read2_b32 v[46:47], v13 offset0:12 offset1:13
	ds_read2_b32 v[50:51], v13 offset0:14 offset1:15
	s_waitcnt lgkmcnt(3)
	v_med3_f32 v4, v42, s33, v39
	v_med3_f32 v43, v43, s33, v39
	v_mov_b32_e32 v42, v5
	v_cvt_pk_fp8_f32 v42, v4, v43
	s_waitcnt lgkmcnt(2)
	v_med3_f32 v4, v44, s33, v39
	v_med3_f32 v44, v45, s33, v39
	s_waitcnt lgkmcnt(1)
	v_med3_f32 v45, v46, s33, v39
	v_med3_f32 v46, v47, s33, v39
	v_mov_b32_e32 v43, v5
	v_cvt_pk_fp8_f32 v43, v45, v46
	v_cvt_pk_fp8_f32 v42, v4, v44 op_sel:[0,0,1]
	s_waitcnt lgkmcnt(0)
	v_med3_f32 v4, v50, s33, v39
	v_med3_f32 v44, v51, s33, v39
	v_cvt_pk_fp8_f32 v43, v4, v44 op_sel:[0,0,1]
	ds_read2_b32 v[44:45], v14 offset1:1
	v_or_b32_e32 v4, s2, v7
	v_lshlrev_b32_e32 v4, 10, v4
	v_lshl_add_u64 v[46:47], v[48:49], 0, v[4:5]
	ds_read2_b32 v[50:51], v15 offset1:1
	ds_read2_b32 v[52:53], v16 offset1:1
	ds_read2_b32 v[54:55], v17 offset1:1
	s_waitcnt lgkmcnt(3)
	v_med3_f32 v4, v44, s33, v39
	v_med3_f32 v45, v45, s33, v39
	v_mov_b32_e32 v44, v5
	v_cvt_pk_fp8_f32 v44, v4, v45
	global_store_dwordx4 v[46:47], v[40:43], off nt
	s_waitcnt lgkmcnt(2)
	v_med3_f32 v4, v50, s33, v39
	v_mov_b32_e32 v45, v5
	v_med3_f32 v40, v51, s33, v39
	v_cvt_pk_fp8_f32 v44, v4, v40 op_sel:[0,0,1]
	s_waitcnt lgkmcnt(1)
	v_med3_f32 v4, v52, s33, v39
	v_med3_f32 v40, v53, s33, v39
	v_cvt_pk_fp8_f32 v45, v4, v40
	ds_read2_b32 v[40:41], v18 offset1:1
	s_waitcnt lgkmcnt(1)
	v_med3_f32 v4, v54, s33, v39
	v_med3_f32 v42, v55, s33, v39
	v_cvt_pk_fp8_f32 v45, v4, v42 op_sel:[0,0,1]
	ds_read2_b32 v[42:43], v19 offset1:1
	ds_read2_b32 v[50:51], v20 offset1:1
	ds_read2_b32 v[52:53], v21 offset1:1
	s_waitcnt lgkmcnt(3)
	v_med3_f32 v4, v40, s33, v39
	v_med3_f32 v40, v41, s33, v39
	v_mov_b32_e32 v46, v5
	v_cvt_pk_fp8_f32 v46, v4, v40
	s_waitcnt lgkmcnt(2)
	v_med3_f32 v4, v42, s33, v39
	s_waitcnt lgkmcnt(1)
	v_med3_f32 v41, v50, s33, v39
	v_med3_f32 v42, v51, s33, v39
	v_mov_b32_e32 v47, v5
	v_cvt_pk_fp8_f32 v47, v41, v42
	v_med3_f32 v40, v43, s33, v39
	v_cvt_pk_fp8_f32 v46, v4, v40 op_sel:[0,0,1]
	s_waitcnt lgkmcnt(0)
	v_med3_f32 v4, v52, s33, v39
	v_med3_f32 v40, v53, s33, v39
	v_cvt_pk_fp8_f32 v47, v4, v40 op_sel:[0,0,1]
	ds_read2_b32 v[40:41], v22 offset1:1
	v_or_b32_e32 v4, s2, v9
	v_lshlrev_b32_e32 v4, 10, v4
	v_lshl_add_u64 v[42:43], v[48:49], 0, v[4:5]
	ds_read2_b32 v[50:51], v23 offset1:1
	ds_read2_b32 v[52:53], v24 offset1:1
	ds_read2_b32 v[54:55], v25 offset1:1
	s_waitcnt lgkmcnt(3)
	v_med3_f32 v4, v40, s33, v39
	v_med3_f32 v41, v41, s33, v39
	v_mov_b32_e32 v40, v5
	v_cvt_pk_fp8_f32 v40, v4, v41
	s_waitcnt lgkmcnt(2)
	v_med3_f32 v4, v50, s33, v39
	v_med3_f32 v41, v51, s33, v39
	global_store_dwordx4 v[42:43], v[44:47], off nt
	v_cvt_pk_fp8_f32 v40, v4, v41 op_sel:[0,0,1]
	s_waitcnt lgkmcnt(1)
	v_med3_f32 v4, v52, s33, v39
	v_med3_f32 v42, v53, s33, v39
	v_mov_b32_e32 v41, v5
	v_cvt_pk_fp8_f32 v41, v4, v42
	ds_read2_b32 v[42:43], v26 offset1:1
	s_waitcnt lgkmcnt(1)
	v_med3_f32 v4, v54, s33, v39
	v_med3_f32 v44, v55, s33, v39
	v_cvt_pk_fp8_f32 v41, v4, v44 op_sel:[0,0,1]
	ds_read2_b32 v[44:45], v27 offset1:1
	ds_read2_b32 v[46:47], v28 offset1:1
	ds_read2_b32 v[50:51], v29 offset1:1
	s_waitcnt lgkmcnt(3)
	v_med3_f32 v4, v42, s33, v39
	v_med3_f32 v43, v43, s33, v39
	v_mov_b32_e32 v42, v5
	v_cvt_pk_fp8_f32 v42, v4, v43
	s_waitcnt lgkmcnt(2)
	v_med3_f32 v4, v44, s33, v39
	v_med3_f32 v44, v45, s33, v39
	s_waitcnt lgkmcnt(1)
	v_med3_f32 v45, v46, s33, v39
	v_med3_f32 v46, v47, s33, v39
	v_mov_b32_e32 v43, v5
	v_cvt_pk_fp8_f32 v43, v45, v46
	v_cvt_pk_fp8_f32 v42, v4, v44 op_sel:[0,0,1]
	s_waitcnt lgkmcnt(0)
	v_med3_f32 v4, v50, s33, v39
	v_med3_f32 v44, v51, s33, v39
	v_cvt_pk_fp8_f32 v43, v4, v44 op_sel:[0,0,1]
	ds_read2_b32 v[44:45], v30 offset1:1
	v_or_b32_e32 v4, s2, v10
	v_lshlrev_b32_e32 v4, 10, v4
	v_lshl_add_u64 v[46:47], v[48:49], 0, v[4:5]
	ds_read2_b32 v[50:51], v31 offset1:1
	ds_read2_b32 v[52:53], v32 offset1:1
	ds_read2_b32 v[54:55], v33 offset1:1
	s_waitcnt lgkmcnt(3)
	v_med3_f32 v4, v44, s33, v39
	v_med3_f32 v45, v45, s33, v39
	v_mov_b32_e32 v44, v5
	v_cvt_pk_fp8_f32 v44, v4, v45
	global_store_dwordx4 v[46:47], v[40:43], off nt
	s_waitcnt lgkmcnt(2)
	v_med3_f32 v4, v50, s33, v39
	v_mov_b32_e32 v45, v5
	v_med3_f32 v40, v51, s33, v39
	v_cvt_pk_fp8_f32 v44, v4, v40 op_sel:[0,0,1]
	s_waitcnt lgkmcnt(1)
	v_med3_f32 v4, v52, s33, v39
	v_med3_f32 v40, v53, s33, v39
	v_cvt_pk_fp8_f32 v45, v4, v40
	ds_read2_b32 v[40:41], v34 offset1:1
	s_waitcnt lgkmcnt(1)
	v_med3_f32 v4, v54, s33, v39
	v_med3_f32 v42, v55, s33, v39
	v_cvt_pk_fp8_f32 v45, v4, v42 op_sel:[0,0,1]
	ds_read2_b32 v[42:43], v35 offset1:1
	ds_read2_b32 v[50:51], v36 offset1:1
	ds_read2_b32 v[52:53], v37 offset1:1
	s_waitcnt lgkmcnt(3)
	v_med3_f32 v4, v40, s33, v39
	v_med3_f32 v40, v41, s33, v39
	v_mov_b32_e32 v46, v5
	v_cvt_pk_fp8_f32 v46, v4, v40
	s_waitcnt lgkmcnt(2)
	v_med3_f32 v4, v42, s33, v39
	s_waitcnt lgkmcnt(1)
	v_med3_f32 v41, v50, s33, v39
	v_med3_f32 v42, v51, s33, v39
	v_mov_b32_e32 v47, v5
	v_cvt_pk_fp8_f32 v47, v41, v42
	v_med3_f32 v40, v43, s33, v39
	v_cvt_pk_fp8_f32 v46, v4, v40 op_sel:[0,0,1]
	s_waitcnt lgkmcnt(0)
	v_med3_f32 v4, v52, s33, v39
	v_med3_f32 v40, v53, s33, v39
	v_cvt_pk_fp8_f32 v47, v4, v40 op_sel:[0,0,1]
	v_or_b32_e32 v4, s2, v11
	v_lshlrev_b32_e32 v4, 10, v4
	v_lshl_add_u64 v[40:41], v[48:49], 0, v[4:5]
	global_store_dwordx4 v[40:41], v[44:47], off nt
	s_waitcnt lgkmcnt(0)
.LBB0_469:
	s_andn2_b64 vcc, exec, s[4:5]
	s_cbranch_vccnz .LBB0_457
	v_readlane_b32 s60, v255, 3
	s_lshr_b32 s2, s6, 9
	v_readlane_b32 s68, v255, 11
	v_readlane_b32 s69, v255, 12
	v_readlane_b32 s70, v255, 13
	v_readlane_b32 s71, v255, 14
	v_readlane_b32 s72, v255, 15
	v_readlane_b32 s73, v255, 16
	s_lshl_b64 s[4:5], s[2:3], 23
	v_readlane_b32 s74, v255, 17
	v_readlane_b32 s75, v255, 18
	s_mov_b64 s[68:69], s[72:73]
	s_add_u32 s44, s68, s4
	s_addc_u32 s45, s69, s5
	s_lshl_b64 s[8:9], s[2:3], 21
	s_add_u32 s5, s12, s8
	s_addc_u32 s4, s13, s9
	s_lshl_b32 s2, s6, 1
	s_and_b32 s8, s2, 0x380
	s_and_b32 s2, s7, 0x7e0
	s_and_b32 s7, s7, 0xe0
	s_cmpk_lt_u32 s7, 0x80
	s_cselect_b64 vcc, -1, 0
	s_lshl_b32 s6, s6, 4
	v_or_b32_e32 v4, s7, v6
	s_and_b32 s6, s6, 0x380
	v_or_b32_e32 v40, s6, v4
	s_addk_i32 s6, 0x380
	v_add_u32_e32 v4, s6, v4
	v_cndmask_b32_e32 v4, v4, v40, vcc
	v_or_b32_e32 v42, s8, v7
	v_lshlrev_b32_e32 v4, 2, v4
	v_lshl_add_u64 v[40:41], s[44:45], 0, v[4:5]
	v_lshlrev_b32_e32 v4, 13, v42
	v_lshl_add_u64 v[96:97], v[40:41], 0, v[4:5]
	v_add_co_u32_e32 v44, vcc, s18, v96
	global_load_dwordx4 v[40:43], v[96:97], off nt
	s_nop 0
	v_addc_co_u32_e32 v45, vcc, 0, v97, vcc
	global_load_dwordx4 v[44:47], v[44:45], off nt
	v_add_co_u32_e32 v48, vcc, s20, v96
	s_add_u32 s6, s5, s8
	s_nop 0
	v_addc_co_u32_e32 v49, vcc, 0, v97, vcc
	v_add_co_u32_e32 v52, vcc, s22, v96
	global_load_dwordx4 v[48:51], v[48:49], off nt
	s_nop 0
	v_addc_co_u32_e32 v53, vcc, 0, v97, vcc
	global_load_dwordx4 v[52:55], v[52:53], off nt
	v_add_co_u32_e32 v56, vcc, s24, v96
	s_addc_u32 s7, s4, 0
	s_nop 0
	v_addc_co_u32_e32 v57, vcc, 0, v97, vcc
	v_add_co_u32_e32 v60, vcc, s26, v96
	global_load_dwordx4 v[56:59], v[56:57], off nt
	s_nop 0
	v_addc_co_u32_e32 v61, vcc, 0, v97, vcc
	global_load_dwordx4 v[60:63], v[60:61], off nt
	v_add_co_u32_e32 v64, vcc, s28, v96
	v_readlane_b32 s61, v255, 4
	s_nop 0
	v_addc_co_u32_e32 v65, vcc, 0, v97, vcc
	v_add_co_u32_e32 v68, vcc, s30, v96
	global_load_dwordx4 v[64:67], v[64:65], off nt
	s_nop 0
	v_addc_co_u32_e32 v69, vcc, 0, v97, vcc
	global_load_dwordx4 v[68:71], v[68:69], off nt
	v_add_co_u32_e32 v72, vcc, s34, v96
	v_readlane_b32 s62, v255, 5
	s_nop 0
	v_addc_co_u32_e32 v73, vcc, 0, v97, vcc
	v_add_co_u32_e32 v76, vcc, s35, v96
	v_readlane_b32 s63, v255, 6
	s_nop 0
	v_addc_co_u32_e32 v77, vcc, 0, v97, vcc
	global_load_dwordx4 v[72:75], v[72:73], off nt
	s_nop 0
	global_load_dwordx4 v[76:79], v[76:77], off nt
	v_add_co_u32_e32 v80, vcc, s38, v96
	v_readlane_b32 s64, v255, 7
	s_nop 0
	v_addc_co_u32_e32 v81, vcc, 0, v97, vcc
	v_add_co_u32_e32 v84, vcc, s39, v96
	v_readlane_b32 s65, v255, 8
	s_nop 0
	v_addc_co_u32_e32 v85, vcc, 0, v97, vcc
	global_load_dwordx4 v[80:83], v[80:81], off nt
	s_nop 0
	global_load_dwordx4 v[84:87], v[84:85], off nt
	v_add_co_u32_e32 v88, vcc, s40, v96
	v_readlane_b32 s66, v255, 9
	s_nop 0
	v_addc_co_u32_e32 v89, vcc, 0, v97, vcc
	v_add_co_u32_e32 v92, vcc, s41, v96
	v_readlane_b32 s67, v255, 10
	s_nop 0
	v_addc_co_u32_e32 v93, vcc, 0, v97, vcc
	global_load_dwordx4 v[88:91], v[88:89], off nt
	s_nop 0
	global_load_dwordx4 v[92:95], v[92:93], off nt
	v_add_co_u32_e32 v98, vcc, s42, v96
	s_mov_b64 s[70:71], s[74:75]
	s_nop 0
	v_addc_co_u32_e32 v99, vcc, 0, v97, vcc
	v_add_co_u32_e32 v100, vcc, s43, v96
	s_waitcnt vmcnt(13)
	v_mul_f32_e32 v4, 0x42800000, v40
	v_addc_co_u32_e32 v101, vcc, 0, v97, vcc
	global_load_dwordx4 v[96:99], v[98:99], off nt
	s_nop 0
	global_load_dwordx4 v[100:103], v[100:101], off nt
	v_mul_f32_e32 v40, 0x42800000, v41
	v_mul_f32_e32 v41, 0x42800000, v42
	v_mul_f32_e32 v42, 0x42800000, v43
	s_waitcnt vmcnt(14)
	v_mul_f32_e32 v43, 0x42800000, v44
	ds_write2_b32 v8, v4, v43 offset1:8
	v_mul_f32_e32 v4, 0x42800000, v45
	ds_write2_b32 v8, v40, v4 offset0:129 offset1:137
	v_mul_f32_e32 v4, 0x42800000, v46
	ds_write2_b32 v38, v41, v4 offset0:2 offset1:10
	v_mul_f32_e32 v4, 0x42800000, v47
	ds_write2_b32 v38, v42, v4 offset0:131 offset1:139
	s_waitcnt vmcnt(13)
	v_mul_f32_e32 v4, 0x42800000, v48
	s_waitcnt vmcnt(12)
	v_mul_f32_e32 v43, 0x42800000, v52
	v_mul_f32_e32 v40, 0x42800000, v49
	ds_write2_b32 v8, v4, v43 offset0:16 offset1:24
	v_mul_f32_e32 v4, 0x42800000, v53
	v_mul_f32_e32 v41, 0x42800000, v50
	ds_write2_b32 v8, v40, v4 offset0:145 offset1:153
	v_mul_f32_e32 v4, 0x42800000, v54
	v_mul_f32_e32 v42, 0x42800000, v51
	ds_write2_b32 v38, v41, v4 offset0:18 offset1:26
	v_mul_f32_e32 v4, 0x42800000, v55
	ds_write2_b32 v38, v42, v4 offset0:147 offset1:155
	s_waitcnt vmcnt(11)
	v_mul_f32_e32 v4, 0x42800000, v56
	s_waitcnt vmcnt(10)
	v_mul_f32_e32 v43, 0x42800000, v60
	v_mul_f32_e32 v40, 0x42800000, v57
	ds_write2_b32 v8, v4, v43 offset0:32 offset1:40
	v_mul_f32_e32 v4, 0x42800000, v61
	v_mul_f32_e32 v41, 0x42800000, v58
	ds_write2_b32 v8, v40, v4 offset0:161 offset1:169
	v_mul_f32_e32 v4, 0x42800000, v62
	v_mul_f32_e32 v42, 0x42800000, v59
	ds_write2_b32 v38, v41, v4 offset0:34 offset1:42
	v_mul_f32_e32 v4, 0x42800000, v63
	ds_write2_b32 v38, v42, v4 offset0:163 offset1:171
	s_waitcnt vmcnt(9)
	v_mul_f32_e32 v4, 0x42800000, v64
	s_waitcnt vmcnt(8)
	v_mul_f32_e32 v43, 0x42800000, v68
	v_mul_f32_e32 v40, 0x42800000, v65
	ds_write2_b32 v8, v4, v43 offset0:48 offset1:56
	v_mul_f32_e32 v4, 0x42800000, v69
	v_mul_f32_e32 v41, 0x42800000, v66
	ds_write2_b32 v8, v40, v4 offset0:177 offset1:185
	v_mul_f32_e32 v4, 0x42800000, v70
	v_mul_f32_e32 v42, 0x42800000, v67
	ds_write2_b32 v38, v41, v4 offset0:50 offset1:58
	v_mul_f32_e32 v4, 0x42800000, v71
	ds_write2_b32 v38, v42, v4 offset0:179 offset1:187
	s_waitcnt vmcnt(7)
	v_mul_f32_e32 v4, 0x42800000, v72
	s_waitcnt vmcnt(6)
	v_mul_f32_e32 v43, 0x42800000, v76
	v_mul_f32_e32 v40, 0x42800000, v73
	ds_write2_b32 v8, v4, v43 offset0:64 offset1:72
	v_mul_f32_e32 v4, 0x42800000, v77
	v_mul_f32_e32 v41, 0x42800000, v74
	ds_write2_b32 v8, v40, v4 offset0:193 offset1:201
	v_mul_f32_e32 v4, 0x42800000, v78
	v_mul_f32_e32 v42, 0x42800000, v75
	ds_write2_b32 v38, v41, v4 offset0:66 offset1:74
	v_mul_f32_e32 v4, 0x42800000, v79
	ds_write2_b32 v38, v42, v4 offset0:195 offset1:203
	s_waitcnt vmcnt(5)
	v_mul_f32_e32 v4, 0x42800000, v80
	s_waitcnt vmcnt(4)
	v_mul_f32_e32 v43, 0x42800000, v84
	v_mul_f32_e32 v40, 0x42800000, v81
	ds_write2_b32 v8, v4, v43 offset0:80 offset1:88
	v_mul_f32_e32 v4, 0x42800000, v85
	v_mul_f32_e32 v41, 0x42800000, v82
	ds_write2_b32 v8, v40, v4 offset0:209 offset1:217
	v_mul_f32_e32 v4, 0x42800000, v86
	v_mul_f32_e32 v42, 0x42800000, v83
	ds_write2_b32 v38, v41, v4 offset0:82 offset1:90
	v_mul_f32_e32 v4, 0x42800000, v87
	ds_write2_b32 v38, v42, v4 offset0:211 offset1:219
	s_waitcnt vmcnt(3)
	v_mul_f32_e32 v4, 0x42800000, v88
	s_waitcnt vmcnt(2)
	v_mul_f32_e32 v43, 0x42800000, v92
	v_mul_f32_e32 v40, 0x42800000, v89
	ds_write2_b32 v8, v4, v43 offset0:96 offset1:104
	v_mul_f32_e32 v4, 0x42800000, v93
	v_mul_f32_e32 v41, 0x42800000, v90
	ds_write2_b32 v8, v40, v4 offset0:225 offset1:233
	v_mul_f32_e32 v4, 0x42800000, v94
	v_mul_f32_e32 v42, 0x42800000, v91
	ds_write2_b32 v38, v41, v4 offset0:98 offset1:106
	v_mul_f32_e32 v4, 0x42800000, v95
	ds_write2_b32 v38, v42, v4 offset0:227 offset1:235
	s_waitcnt vmcnt(1)
	v_mul_f32_e32 v4, 0x42800000, v96
	s_waitcnt vmcnt(0)
	v_mul_f32_e32 v43, 0x42800000, v100
	v_mul_f32_e32 v40, 0x42800000, v97
	ds_write2_b32 v8, v4, v43 offset0:112 offset1:120
	v_mul_f32_e32 v4, 0x42800000, v101
	v_mul_f32_e32 v41, 0x42800000, v98
	ds_write2_b32 v8, v40, v4 offset0:241 offset1:249
	v_mul_f32_e32 v4, 0x42800000, v102
	v_mul_f32_e32 v42, 0x42800000, v99
	ds_write2_b32 v38, v41, v4 offset0:114 offset1:122
	v_mul_f32_e32 v4, 0x42800000, v103
	ds_write2_b32 v38, v42, v4 offset0:243 offset1:251
	s_waitcnt lgkmcnt(0)
	ds_read2_b32 v[40:41], v13 offset1:1
	ds_read2_b32 v[42:43], v13 offset0:2 offset1:3
	ds_read2_b32 v[44:45], v13 offset0:4 offset1:5
	ds_read2_b32 v[46:47], v13 offset0:6 offset1:7
	v_lshl_add_u64 v[48:49], s[6:7], 0, v[2:3]
	s_waitcnt lgkmcnt(3)
	v_med3_f32 v4, v40, s33, v39
	v_med3_f32 v41, v41, s33, v39
	v_mov_b32_e32 v40, v5
	v_cvt_pk_fp8_f32 v40, v4, v41
	s_waitcnt lgkmcnt(2)
	v_med3_f32 v4, v42, s33, v39
	v_med3_f32 v41, v43, s33, v39
	s_waitcnt lgkmcnt(1)
	v_med3_f32 v42, v45, s33, v39
	v_cvt_pk_fp8_f32 v40, v4, v41 op_sel:[0,0,1]
	v_med3_f32 v4, v44, s33, v39
	v_mov_b32_e32 v41, v5
	v_cvt_pk_fp8_f32 v41, v4, v42
	ds_read2_b32 v[42:43], v13 offset0:8 offset1:9
	s_waitcnt lgkmcnt(1)
	v_med3_f32 v4, v46, s33, v39
	v_med3_f32 v44, v47, s33, v39
	v_cvt_pk_fp8_f32 v41, v4, v44 op_sel:[0,0,1]
	ds_read2_b32 v[44:45], v13 offset0:10 offset1:11
	ds_read2_b32 v[46:47], v13 offset0:12 offset1:13
	ds_read2_b32 v[50:51], v13 offset0:14 offset1:15
	s_waitcnt lgkmcnt(3)
	v_med3_f32 v4, v42, s33, v39
	v_med3_f32 v43, v43, s33, v39
	v_mov_b32_e32 v42, v5
	v_cvt_pk_fp8_f32 v42, v4, v43
	s_waitcnt lgkmcnt(2)
	v_med3_f32 v4, v44, s33, v39
	v_med3_f32 v44, v45, s33, v39
	s_waitcnt lgkmcnt(1)
	v_med3_f32 v45, v46, s33, v39
	v_med3_f32 v46, v47, s33, v39
	v_mov_b32_e32 v43, v5
	v_cvt_pk_fp8_f32 v43, v45, v46
	v_cvt_pk_fp8_f32 v42, v4, v44 op_sel:[0,0,1]
	s_waitcnt lgkmcnt(0)
	v_med3_f32 v4, v50, s33, v39
	v_med3_f32 v44, v51, s33, v39
	v_cvt_pk_fp8_f32 v43, v4, v44 op_sel:[0,0,1]
	ds_read2_b32 v[44:45], v14 offset1:1
	v_or_b32_e32 v4, s2, v7
	v_lshlrev_b32_e32 v4, 10, v4
	v_lshl_add_u64 v[46:47], v[48:49], 0, v[4:5]
	ds_read2_b32 v[50:51], v15 offset1:1
	ds_read2_b32 v[52:53], v16 offset1:1
	ds_read2_b32 v[54:55], v17 offset1:1
	s_waitcnt lgkmcnt(3)
	v_med3_f32 v4, v44, s33, v39
	v_med3_f32 v45, v45, s33, v39
	v_mov_b32_e32 v44, v5
	v_cvt_pk_fp8_f32 v44, v4, v45
	global_store_dwordx4 v[46:47], v[40:43], off nt
	s_waitcnt lgkmcnt(2)
	v_med3_f32 v4, v50, s33, v39
	v_mov_b32_e32 v45, v5
	v_med3_f32 v40, v51, s33, v39
	v_cvt_pk_fp8_f32 v44, v4, v40 op_sel:[0,0,1]
	s_waitcnt lgkmcnt(1)
	v_med3_f32 v4, v52, s33, v39
	v_med3_f32 v40, v53, s33, v39
	v_cvt_pk_fp8_f32 v45, v4, v40
	ds_read2_b32 v[40:41], v18 offset1:1
	s_waitcnt lgkmcnt(1)
	v_med3_f32 v4, v54, s33, v39
	v_med3_f32 v42, v55, s33, v39
	v_cvt_pk_fp8_f32 v45, v4, v42 op_sel:[0,0,1]
	ds_read2_b32 v[42:43], v19 offset1:1
	ds_read2_b32 v[50:51], v20 offset1:1
	ds_read2_b32 v[52:53], v21 offset1:1
	s_waitcnt lgkmcnt(3)
	v_med3_f32 v4, v40, s33, v39
	v_med3_f32 v40, v41, s33, v39
	v_mov_b32_e32 v46, v5
	v_cvt_pk_fp8_f32 v46, v4, v40
	s_waitcnt lgkmcnt(2)
	v_med3_f32 v4, v42, s33, v39
	s_waitcnt lgkmcnt(1)
	v_med3_f32 v41, v50, s33, v39
	v_med3_f32 v42, v51, s33, v39
	v_mov_b32_e32 v47, v5
	v_cvt_pk_fp8_f32 v47, v41, v42
	v_med3_f32 v40, v43, s33, v39
	v_cvt_pk_fp8_f32 v46, v4, v40 op_sel:[0,0,1]
	s_waitcnt lgkmcnt(0)
	v_med3_f32 v4, v52, s33, v39
	v_med3_f32 v40, v53, s33, v39
	v_cvt_pk_fp8_f32 v47, v4, v40 op_sel:[0,0,1]
	ds_read2_b32 v[40:41], v22 offset1:1
	v_or_b32_e32 v4, s2, v9
	v_lshlrev_b32_e32 v4, 10, v4
	v_lshl_add_u64 v[42:43], v[48:49], 0, v[4:5]
	ds_read2_b32 v[50:51], v23 offset1:1
	ds_read2_b32 v[52:53], v24 offset1:1
	ds_read2_b32 v[54:55], v25 offset1:1
	s_waitcnt lgkmcnt(3)
	v_med3_f32 v4, v40, s33, v39
	v_med3_f32 v41, v41, s33, v39
	v_mov_b32_e32 v40, v5
	v_cvt_pk_fp8_f32 v40, v4, v41
	s_waitcnt lgkmcnt(2)
	v_med3_f32 v4, v50, s33, v39
	v_med3_f32 v41, v51, s33, v39
	global_store_dwordx4 v[42:43], v[44:47], off nt
	v_cvt_pk_fp8_f32 v40, v4, v41 op_sel:[0,0,1]
	s_waitcnt lgkmcnt(1)
	v_med3_f32 v4, v52, s33, v39
	v_med3_f32 v42, v53, s33, v39
	v_mov_b32_e32 v41, v5
	v_cvt_pk_fp8_f32 v41, v4, v42
	ds_read2_b32 v[42:43], v26 offset1:1
	s_waitcnt lgkmcnt(1)
	v_med3_f32 v4, v54, s33, v39
	v_med3_f32 v44, v55, s33, v39
	v_cvt_pk_fp8_f32 v41, v4, v44 op_sel:[0,0,1]
	ds_read2_b32 v[44:45], v27 offset1:1
	ds_read2_b32 v[46:47], v28 offset1:1
	ds_read2_b32 v[50:51], v29 offset1:1
	s_waitcnt lgkmcnt(3)
	v_med3_f32 v4, v42, s33, v39
	v_med3_f32 v43, v43, s33, v39
	v_mov_b32_e32 v42, v5
	v_cvt_pk_fp8_f32 v42, v4, v43
	s_waitcnt lgkmcnt(2)
	v_med3_f32 v4, v44, s33, v39
	v_med3_f32 v44, v45, s33, v39
	s_waitcnt lgkmcnt(1)
	v_med3_f32 v45, v46, s33, v39
	v_med3_f32 v46, v47, s33, v39
	v_mov_b32_e32 v43, v5
	v_cvt_pk_fp8_f32 v43, v45, v46
	v_cvt_pk_fp8_f32 v42, v4, v44 op_sel:[0,0,1]
	s_waitcnt lgkmcnt(0)
	v_med3_f32 v4, v50, s33, v39
	v_med3_f32 v44, v51, s33, v39
	v_cvt_pk_fp8_f32 v43, v4, v44 op_sel:[0,0,1]
	ds_read2_b32 v[44:45], v30 offset1:1
	v_or_b32_e32 v4, s2, v10
	v_lshlrev_b32_e32 v4, 10, v4
	v_lshl_add_u64 v[46:47], v[48:49], 0, v[4:5]
	ds_read2_b32 v[50:51], v31 offset1:1
	ds_read2_b32 v[52:53], v32 offset1:1
	ds_read2_b32 v[54:55], v33 offset1:1
	s_waitcnt lgkmcnt(3)
	v_med3_f32 v4, v44, s33, v39
	v_med3_f32 v45, v45, s33, v39
	v_mov_b32_e32 v44, v5
	v_cvt_pk_fp8_f32 v44, v4, v45
	global_store_dwordx4 v[46:47], v[40:43], off nt
	s_waitcnt lgkmcnt(2)
	v_med3_f32 v4, v50, s33, v39
	v_mov_b32_e32 v45, v5
	v_med3_f32 v40, v51, s33, v39
	v_cvt_pk_fp8_f32 v44, v4, v40 op_sel:[0,0,1]
	s_waitcnt lgkmcnt(1)
	v_med3_f32 v4, v52, s33, v39
	v_med3_f32 v40, v53, s33, v39
	v_cvt_pk_fp8_f32 v45, v4, v40
	ds_read2_b32 v[40:41], v34 offset1:1
	s_waitcnt lgkmcnt(1)
	v_med3_f32 v4, v54, s33, v39
	v_med3_f32 v42, v55, s33, v39
	v_cvt_pk_fp8_f32 v45, v4, v42 op_sel:[0,0,1]
	ds_read2_b32 v[42:43], v35 offset1:1
	ds_read2_b32 v[50:51], v36 offset1:1
	ds_read2_b32 v[52:53], v37 offset1:1
	s_waitcnt lgkmcnt(3)
	v_med3_f32 v4, v40, s33, v39
	v_med3_f32 v40, v41, s33, v39
	v_mov_b32_e32 v46, v5
	v_cvt_pk_fp8_f32 v46, v4, v40
	s_waitcnt lgkmcnt(2)
	v_med3_f32 v4, v42, s33, v39
	s_waitcnt lgkmcnt(1)
	v_med3_f32 v41, v50, s33, v39
	v_med3_f32 v42, v51, s33, v39
	v_mov_b32_e32 v47, v5
	v_cvt_pk_fp8_f32 v47, v41, v42
	v_med3_f32 v40, v43, s33, v39
	v_cvt_pk_fp8_f32 v46, v4, v40 op_sel:[0,0,1]
	s_waitcnt lgkmcnt(0)
	v_med3_f32 v4, v52, s33, v39
	v_med3_f32 v40, v53, s33, v39
	v_cvt_pk_fp8_f32 v47, v4, v40 op_sel:[0,0,1]
	v_or_b32_e32 v4, s2, v11
	v_lshlrev_b32_e32 v4, 10, v4
	v_lshl_add_u64 v[40:41], v[48:49], 0, v[4:5]
	global_store_dwordx4 v[40:41], v[44:47], off nt
	s_waitcnt lgkmcnt(0)
	s_branch .LBB0_457

.LBB0_627:
	s_or_b64 exec, exec, s[4:5]
	s_waitcnt lgkmcnt(0)
	s_barrier
	ds_read_b32 v4, v12
	s_mov_b64 s[4:5], -1
	s_waitcnt lgkmcnt(0)
	v_cmp_lt_u32_e32 vcc, s17, v4
	v_readfirstlane_b32 s2, v4
	s_cbranch_vccnz .LBB0_620
	s_lshl_b32 s6, s2, 3
	s_add_i32 s6, s6, s91
	s_cmpk_gt_u32 s6, 0x5fff
	s_cbranch_scc1 .LBB0_619
	s_lshl_b32 s7, s6, 5
	s_cmpk_gt_u32 s6, 0x3fff
	s_cbranch_scc0 .LBB0_631
	s_add_i32 s2, s6, 0xffffc000
	s_lshr_b32 s2, s2, 8
	s_lshl_b64 s[4:5], s[2:3], 20
	s_lshl_b64 s[8:9], s[2:3], 22
	s_add_u32 s8, s76, s8
	s_addc_u32 s9, s77, s9
	s_add_u32 s4, s10, s4
	s_addc_u32 s5, s11, s5
	s_lshl_b32 s2, s6, 2
	s_and_b32 s45, s2, 0x380
	s_and_b32 s2, s7, 0x3e0
	v_or_b32_e32 v4, s2, v7
	v_or_b32_e32 v42, s45, v1
	v_lshlrev_b32_e32 v4, 2, v4
	v_lshl_add_u64 v[40:41], s[8:9], 0, v[4:5]
	v_lshlrev_b32_e32 v4, 12, v42
	v_lshl_add_u64 v[96:97], v[40:41], 0, v[4:5]
	v_add_co_u32_e32 v44, vcc, s18, v96
	global_load_dwordx4 v[40:43], v[96:97], off nt
	s_nop 0
	v_addc_co_u32_e32 v45, vcc, 0, v97, vcc
	global_load_dwordx4 v[44:47], v[44:45], off nt
	v_add_co_u32_e32 v48, vcc, s19, v96
	s_add_u32 s4, s4, s45
	s_nop 0
	v_addc_co_u32_e32 v49, vcc, 0, v97, vcc
	v_add_co_u32_e32 v52, vcc, s20, v96
	global_load_dwordx4 v[48:51], v[48:49], off nt
	s_nop 0
	v_addc_co_u32_e32 v53, vcc, 0, v97, vcc
	global_load_dwordx4 v[52:55], v[52:53], off nt
	v_add_co_u32_e32 v56, vcc, s21, v96
	s_addc_u32 s5, s5, 0
	s_nop 0
	v_addc_co_u32_e32 v57, vcc, 0, v97, vcc
	v_add_co_u32_e32 v60, vcc, s22, v96
	global_load_dwordx4 v[56:59], v[56:57], off nt
	s_nop 0
	v_addc_co_u32_e32 v61, vcc, 0, v97, vcc
	global_load_dwordx4 v[60:63], v[60:61], off nt
	v_add_co_u32_e32 v64, vcc, s23, v96
	s_nop 1
	v_addc_co_u32_e32 v65, vcc, 0, v97, vcc
	v_add_co_u32_e32 v68, vcc, s24, v96
	global_load_dwordx4 v[64:67], v[64:65], off nt
	s_nop 0
	v_addc_co_u32_e32 v69, vcc, 0, v97, vcc
	global_load_dwordx4 v[68:71], v[68:69], off nt
	v_add_co_u32_e32 v72, vcc, s25, v96
	s_waitcnt vmcnt(7)
	v_mul_f32_e32 v4, 0x42800000, v40
	v_addc_co_u32_e32 v73, vcc, 0, v97, vcc
	v_add_co_u32_e32 v76, vcc, s26, v96
	v_mul_f32_e32 v40, 0x42800000, v41
	s_nop 0
	v_addc_co_u32_e32 v77, vcc, 0, v97, vcc
	global_load_dwordx4 v[72:75], v[72:73], off nt
	s_nop 0
	global_load_dwordx4 v[76:79], v[76:77], off nt
	v_add_co_u32_e32 v80, vcc, s27, v96
	v_mul_f32_e32 v41, 0x42800000, v42
	s_nop 0
	v_addc_co_u32_e32 v81, vcc, 0, v97, vcc
	v_add_co_u32_e32 v84, vcc, s28, v96
	v_mul_f32_e32 v42, 0x42800000, v43
	s_nop 0
	v_addc_co_u32_e32 v85, vcc, 0, v97, vcc
	global_load_dwordx4 v[80:83], v[80:81], off nt
	s_nop 0
	global_load_dwordx4 v[84:87], v[84:85], off nt
	v_add_co_u32_e32 v88, vcc, s29, v96
	s_waitcnt vmcnt(10)
	v_mul_f32_e32 v43, 0x42800000, v44
	v_addc_co_u32_e32 v89, vcc, 0, v97, vcc
	v_add_co_u32_e32 v92, vcc, s30, v96
	s_nop 1
	v_addc_co_u32_e32 v93, vcc, 0, v97, vcc
	global_load_dwordx4 v[88:91], v[88:89], off nt
	s_nop 0
	global_load_dwordx4 v[92:95], v[92:93], off nt
	v_add_co_u32_e32 v98, vcc, s31, v96
	s_nop 1
	v_addc_co_u32_e32 v99, vcc, 0, v97, vcc
	v_add_co_u32_e32 v100, vcc, s33, v96
	s_nop 1
	v_addc_co_u32_e32 v101, vcc, 0, v97, vcc
	global_load_dwordx4 v[96:99], v[98:99], off nt
	s_nop 0
	global_load_dwordx4 v[100:103], v[100:101], off nt
	ds_write2_b32 v8, v4, v43 offset1:8
	v_mul_f32_e32 v4, 0x42800000, v45
	ds_write2_b32 v8, v40, v4 offset0:129 offset1:137
	v_mul_f32_e32 v4, 0x42800000, v46
	ds_write2_b32 v38, v41, v4 offset0:2 offset1:10
	v_mul_f32_e32 v4, 0x42800000, v47
	ds_write2_b32 v38, v42, v4 offset0:131 offset1:139
	s_waitcnt vmcnt(13)
	v_mul_f32_e32 v4, 0x42800000, v48
	s_waitcnt vmcnt(12)
	v_mul_f32_e32 v43, 0x42800000, v52
	v_mul_f32_e32 v40, 0x42800000, v49
	ds_write2_b32 v8, v4, v43 offset0:16 offset1:24
	v_mul_f32_e32 v4, 0x42800000, v53
	v_mul_f32_e32 v41, 0x42800000, v50
	ds_write2_b32 v8, v40, v4 offset0:145 offset1:153
	v_mul_f32_e32 v4, 0x42800000, v54
	v_mul_f32_e32 v42, 0x42800000, v51
	ds_write2_b32 v38, v41, v4 offset0:18 offset1:26
	v_mul_f32_e32 v4, 0x42800000, v55
	ds_write2_b32 v38, v42, v4 offset0:147 offset1:155
	s_waitcnt vmcnt(11)
	v_mul_f32_e32 v4, 0x42800000, v56
	s_waitcnt vmcnt(10)
	v_mul_f32_e32 v43, 0x42800000, v60
	v_mul_f32_e32 v40, 0x42800000, v57
	ds_write2_b32 v8, v4, v43 offset0:32 offset1:40
	v_mul_f32_e32 v4, 0x42800000, v61
	v_mul_f32_e32 v41, 0x42800000, v58
	ds_write2_b32 v8, v40, v4 offset0:161 offset1:169
	v_mul_f32_e32 v4, 0x42800000, v62
	v_mul_f32_e32 v42, 0x42800000, v59
	ds_write2_b32 v38, v41, v4 offset0:34 offset1:42
	v_mul_f32_e32 v4, 0x42800000, v63
	ds_write2_b32 v38, v42, v4 offset0:163 offset1:171
	s_waitcnt vmcnt(9)
	v_mul_f32_e32 v4, 0x42800000, v64
	s_waitcnt vmcnt(8)
	v_mul_f32_e32 v43, 0x42800000, v68
	v_mul_f32_e32 v40, 0x42800000, v65
	ds_write2_b32 v8, v4, v43 offset0:48 offset1:56
	v_mul_f32_e32 v4, 0x42800000, v69
	v_mul_f32_e32 v41, 0x42800000, v66
	ds_write2_b32 v8, v40, v4 offset0:177 offset1:185
	v_mul_f32_e32 v4, 0x42800000, v70
	v_mul_f32_e32 v42, 0x42800000, v67
	ds_write2_b32 v38, v41, v4 offset0:50 offset1:58
	v_mul_f32_e32 v4, 0x42800000, v71
	ds_write2_b32 v38, v42, v4 offset0:179 offset1:187
	v_lshl_add_u64 v[48:49], s[4:5], 0, v[2:3]
	s_mov_b64 s[4:5], 0
	s_waitcnt vmcnt(7)
	v_mul_f32_e32 v4, 0x42800000, v72
	s_waitcnt vmcnt(6)
	v_mul_f32_e32 v43, 0x42800000, v76
	v_mul_f32_e32 v40, 0x42800000, v73
	ds_write2_b32 v8, v4, v43 offset0:64 offset1:72
	v_mul_f32_e32 v4, 0x42800000, v77
	v_mul_f32_e32 v41, 0x42800000, v74
	ds_write2_b32 v8, v40, v4 offset0:193 offset1:201
	v_mul_f32_e32 v4, 0x42800000, v78
	v_mul_f32_e32 v42, 0x42800000, v75
	ds_write2_b32 v38, v41, v4 offset0:66 offset1:74
	v_mul_f32_e32 v4, 0x42800000, v79
	ds_write2_b32 v38, v42, v4 offset0:195 offset1:203
	s_waitcnt vmcnt(5)
	v_mul_f32_e32 v4, 0x42800000, v80
	s_waitcnt vmcnt(4)
	v_mul_f32_e32 v43, 0x42800000, v84
	v_mul_f32_e32 v40, 0x42800000, v81
	ds_write2_b32 v8, v4, v43 offset0:80 offset1:88
	v_mul_f32_e32 v4, 0x42800000, v85
	v_mul_f32_e32 v41, 0x42800000, v82
	ds_write2_b32 v8, v40, v4 offset0:209 offset1:217
	v_mul_f32_e32 v4, 0x42800000, v86
	v_mul_f32_e32 v42, 0x42800000, v83
	ds_write2_b32 v38, v41, v4 offset0:82 offset1:90
	v_mul_f32_e32 v4, 0x42800000, v87
	ds_write2_b32 v38, v42, v4 offset0:211 offset1:219
	s_waitcnt vmcnt(3)
	v_mul_f32_e32 v4, 0x42800000, v88
	s_waitcnt vmcnt(2)
	v_mul_f32_e32 v43, 0x42800000, v92
	v_mul_f32_e32 v40, 0x42800000, v89
	ds_write2_b32 v8, v4, v43 offset0:96 offset1:104
	v_mul_f32_e32 v4, 0x42800000, v93
	v_mul_f32_e32 v41, 0x42800000, v90
	ds_write2_b32 v8, v40, v4 offset0:225 offset1:233
	v_mul_f32_e32 v4, 0x42800000, v94
	v_mul_f32_e32 v42, 0x42800000, v91
	ds_write2_b32 v38, v41, v4 offset0:98 offset1:106
	v_mul_f32_e32 v4, 0x42800000, v95
	ds_write2_b32 v38, v42, v4 offset0:227 offset1:235
	s_waitcnt vmcnt(1)
	v_mul_f32_e32 v4, 0x42800000, v96
	s_waitcnt vmcnt(0)
	v_mul_f32_e32 v43, 0x42800000, v100
	v_mul_f32_e32 v40, 0x42800000, v97
	ds_write2_b32 v8, v4, v43 offset0:112 offset1:120
	v_mul_f32_e32 v4, 0x42800000, v101
	v_mul_f32_e32 v41, 0x42800000, v98
	ds_write2_b32 v8, v40, v4 offset0:241 offset1:249
	v_mul_f32_e32 v4, 0x42800000, v102
	v_mul_f32_e32 v42, 0x42800000, v99
	ds_write2_b32 v38, v41, v4 offset0:114 offset1:122
	v_mul_f32_e32 v4, 0x42800000, v103
	ds_write2_b32 v38, v42, v4 offset0:243 offset1:251
	s_waitcnt lgkmcnt(0)
	ds_read2_b32 v[40:41], v13 offset1:1
	ds_read2_b32 v[42:43], v13 offset0:2 offset1:3
	ds_read2_b32 v[44:45], v13 offset0:4 offset1:5
	ds_read2_b32 v[46:47], v13 offset0:6 offset1:7
	s_waitcnt lgkmcnt(3)
	v_med3_f32 v4, v40, s34, v39
	v_med3_f32 v41, v41, s34, v39
	v_mov_b32_e32 v40, v5
	v_cvt_pk_fp8_f32 v40, v4, v41
	s_waitcnt lgkmcnt(2)
	v_med3_f32 v4, v42, s34, v39
	v_med3_f32 v41, v43, s34, v39
	s_waitcnt lgkmcnt(1)
	v_med3_f32 v42, v45, s34, v39
	v_cvt_pk_fp8_f32 v40, v4, v41 op_sel:[0,0,1]
	v_med3_f32 v4, v44, s34, v39
	v_mov_b32_e32 v41, v5
	v_cvt_pk_fp8_f32 v41, v4, v42
	ds_read2_b32 v[42:43], v13 offset0:8 offset1:9
	s_waitcnt lgkmcnt(1)
	v_med3_f32 v4, v46, s34, v39
	v_med3_f32 v44, v47, s34, v39
	v_cvt_pk_fp8_f32 v41, v4, v44 op_sel:[0,0,1]
	ds_read2_b32 v[44:45], v13 offset0:10 offset1:11
	ds_read2_b32 v[46:47], v13 offset0:12 offset1:13
	ds_read2_b32 v[50:51], v13 offset0:14 offset1:15
	s_waitcnt lgkmcnt(3)
	v_med3_f32 v4, v42, s34, v39
	v_med3_f32 v43, v43, s34, v39
	v_mov_b32_e32 v42, v5
	v_cvt_pk_fp8_f32 v42, v4, v43
	s_waitcnt lgkmcnt(2)
	v_med3_f32 v4, v44, s34, v39
	v_med3_f32 v44, v45, s34, v39
	s_waitcnt lgkmcnt(1)
	v_med3_f32 v45, v46, s34, v39
	v_med3_f32 v46, v47, s34, v39
	v_mov_b32_e32 v43, v5
	v_cvt_pk_fp8_f32 v43, v45, v46
	v_cvt_pk_fp8_f32 v42, v4, v44 op_sel:[0,0,1]
	s_waitcnt lgkmcnt(0)
	v_med3_f32 v4, v50, s34, v39
	v_med3_f32 v44, v51, s34, v39
	v_cvt_pk_fp8_f32 v43, v4, v44 op_sel:[0,0,1]
	ds_read2_b32 v[44:45], v14 offset1:1
	v_or_b32_e32 v4, s2, v1
	v_lshlrev_b32_e32 v4, 10, v4
	v_lshl_add_u64 v[46:47], v[48:49], 0, v[4:5]
	ds_read2_b32 v[50:51], v15 offset1:1
	ds_read2_b32 v[52:53], v16 offset1:1
	ds_read2_b32 v[54:55], v17 offset1:1
	s_waitcnt lgkmcnt(3)
	v_med3_f32 v4, v44, s34, v39
	v_med3_f32 v45, v45, s34, v39
	v_mov_b32_e32 v44, v5
	v_cvt_pk_fp8_f32 v44, v4, v45
	global_store_dwordx4 v[46:47], v[40:43], off nt
	s_waitcnt lgkmcnt(2)
	v_med3_f32 v4, v50, s34, v39
	v_mov_b32_e32 v45, v5
	v_med3_f32 v40, v51, s34, v39
	v_cvt_pk_fp8_f32 v44, v4, v40 op_sel:[0,0,1]
	s_waitcnt lgkmcnt(1)
	v_med3_f32 v4, v52, s34, v39
	v_med3_f32 v40, v53, s34, v39
	v_cvt_pk_fp8_f32 v45, v4, v40
	ds_read2_b32 v[40:41], v18 offset1:1
	s_waitcnt lgkmcnt(1)
	v_med3_f32 v4, v54, s34, v39
	v_med3_f32 v42, v55, s34, v39
	v_cvt_pk_fp8_f32 v45, v4, v42 op_sel:[0,0,1]
	ds_read2_b32 v[42:43], v19 offset1:1
	ds_read2_b32 v[50:51], v20 offset1:1
	ds_read2_b32 v[52:53], v21 offset1:1
	s_waitcnt lgkmcnt(3)
	v_med3_f32 v4, v40, s34, v39
	v_med3_f32 v40, v41, s34, v39
	v_mov_b32_e32 v46, v5
	v_cvt_pk_fp8_f32 v46, v4, v40
	s_waitcnt lgkmcnt(2)
	v_med3_f32 v4, v42, s34, v39
	s_waitcnt lgkmcnt(1)
	v_med3_f32 v41, v50, s34, v39
	v_med3_f32 v42, v51, s34, v39
	v_mov_b32_e32 v47, v5
	v_cvt_pk_fp8_f32 v47, v41, v42
	v_med3_f32 v40, v43, s34, v39
	v_cvt_pk_fp8_f32 v46, v4, v40 op_sel:[0,0,1]
	s_waitcnt lgkmcnt(0)
	v_med3_f32 v4, v52, s34, v39
	v_med3_f32 v40, v53, s34, v39
	v_cvt_pk_fp8_f32 v47, v4, v40 op_sel:[0,0,1]
	ds_read2_b32 v[40:41], v22 offset1:1
	v_or_b32_e32 v4, s2, v9
	v_lshlrev_b32_e32 v4, 10, v4
	v_lshl_add_u64 v[42:43], v[48:49], 0, v[4:5]
	ds_read2_b32 v[50:51], v23 offset1:1
	ds_read2_b32 v[52:53], v24 offset1:1
	ds_read2_b32 v[54:55], v25 offset1:1
	s_waitcnt lgkmcnt(3)
	v_med3_f32 v4, v40, s34, v39
	v_med3_f32 v41, v41, s34, v39
	v_mov_b32_e32 v40, v5
	v_cvt_pk_fp8_f32 v40, v4, v41
	s_waitcnt lgkmcnt(2)
	v_med3_f32 v4, v50, s34, v39
	v_med3_f32 v41, v51, s34, v39
	global_store_dwordx4 v[42:43], v[44:47], off nt
	v_cvt_pk_fp8_f32 v40, v4, v41 op_sel:[0,0,1]
	s_waitcnt lgkmcnt(1)
	v_med3_f32 v4, v52, s34, v39
	v_med3_f32 v42, v53, s34, v39
	v_mov_b32_e32 v41, v5
	v_cvt_pk_fp8_f32 v41, v4, v42
	ds_read2_b32 v[42:43], v26 offset1:1
	s_waitcnt lgkmcnt(1)
	v_med3_f32 v4, v54, s34, v39
	v_med3_f32 v44, v55, s34, v39
	v_cvt_pk_fp8_f32 v41, v4, v44 op_sel:[0,0,1]
	ds_read2_b32 v[44:45], v27 offset1:1
	ds_read2_b32 v[46:47], v28 offset1:1
	ds_read2_b32 v[50:51], v29 offset1:1
	s_waitcnt lgkmcnt(3)
	v_med3_f32 v4, v42, s34, v39
	v_med3_f32 v43, v43, s34, v39
	v_mov_b32_e32 v42, v5
	v_cvt_pk_fp8_f32 v42, v4, v43
	s_waitcnt lgkmcnt(2)
	v_med3_f32 v4, v44, s34, v39
	v_med3_f32 v44, v45, s34, v39
	s_waitcnt lgkmcnt(1)
	v_med3_f32 v45, v46, s34, v39
	v_med3_f32 v46, v47, s34, v39
	v_mov_b32_e32 v43, v5
	v_cvt_pk_fp8_f32 v43, v45, v46
	v_cvt_pk_fp8_f32 v42, v4, v44 op_sel:[0,0,1]
	s_waitcnt lgkmcnt(0)
	v_med3_f32 v4, v50, s34, v39
	v_med3_f32 v44, v51, s34, v39
	v_cvt_pk_fp8_f32 v43, v4, v44 op_sel:[0,0,1]
	ds_read2_b32 v[44:45], v30 offset1:1
	v_or_b32_e32 v4, s2, v10
	v_lshlrev_b32_e32 v4, 10, v4
	v_lshl_add_u64 v[46:47], v[48:49], 0, v[4:5]
	ds_read2_b32 v[50:51], v31 offset1:1
	ds_read2_b32 v[52:53], v32 offset1:1
	ds_read2_b32 v[54:55], v33 offset1:1
	s_waitcnt lgkmcnt(3)
	v_med3_f32 v4, v44, s34, v39
	v_med3_f32 v45, v45, s34, v39
	v_mov_b32_e32 v44, v5
	v_cvt_pk_fp8_f32 v44, v4, v45
	global_store_dwordx4 v[46:47], v[40:43], off nt
	s_waitcnt lgkmcnt(2)
	v_med3_f32 v4, v50, s34, v39
	v_mov_b32_e32 v45, v5
	v_med3_f32 v40, v51, s34, v39
	v_cvt_pk_fp8_f32 v44, v4, v40 op_sel:[0,0,1]
	s_waitcnt lgkmcnt(1)
	v_med3_f32 v4, v52, s34, v39
	v_med3_f32 v40, v53, s34, v39
	v_cvt_pk_fp8_f32 v45, v4, v40
	ds_read2_b32 v[40:41], v34 offset1:1
	s_waitcnt lgkmcnt(1)
	v_med3_f32 v4, v54, s34, v39
	v_med3_f32 v42, v55, s34, v39
	v_cvt_pk_fp8_f32 v45, v4, v42 op_sel:[0,0,1]
	ds_read2_b32 v[42:43], v35 offset1:1
	ds_read2_b32 v[50:51], v36 offset1:1
	ds_read2_b32 v[52:53], v37 offset1:1
	s_waitcnt lgkmcnt(3)
	v_med3_f32 v4, v40, s34, v39
	v_med3_f32 v40, v41, s34, v39
	v_mov_b32_e32 v46, v5
	v_cvt_pk_fp8_f32 v46, v4, v40
	s_waitcnt lgkmcnt(2)
	v_med3_f32 v4, v42, s34, v39
	s_waitcnt lgkmcnt(1)
	v_med3_f32 v41, v50, s34, v39
	v_med3_f32 v42, v51, s34, v39
	v_mov_b32_e32 v47, v5
	v_cvt_pk_fp8_f32 v47, v41, v42
	v_med3_f32 v40, v43, s34, v39
	v_cvt_pk_fp8_f32 v46, v4, v40 op_sel:[0,0,1]
	s_waitcnt lgkmcnt(0)
	v_med3_f32 v4, v52, s34, v39
	v_med3_f32 v40, v53, s34, v39
	v_cvt_pk_fp8_f32 v47, v4, v40 op_sel:[0,0,1]
	v_or_b32_e32 v4, s2, v11
	v_lshlrev_b32_e32 v4, 10, v4
	v_lshl_add_u64 v[40:41], v[48:49], 0, v[4:5]
	global_store_dwordx4 v[40:41], v[44:47], off nt
	s_waitcnt lgkmcnt(0)
.LBB0_631:
	s_andn2_b64 vcc, exec, s[4:5]
	s_cbranch_vccnz .LBB0_619
	v_readlane_b32 s60, v255, 3
	s_lshr_b32 s2, s6, 9
	v_readlane_b32 s72, v255, 15
	v_readlane_b32 s73, v255, 16
	s_lshl_b64 s[4:5], s[2:3], 23
	v_readlane_b32 s74, v255, 17
	v_readlane_b32 s75, v255, 18
	s_mov_b64 s[52:53], s[72:73]
	s_add_u32 s46, s52, s4
	s_addc_u32 s47, s53, s5
	s_lshl_b64 s[8:9], s[2:3], 21
	s_add_u32 s5, s12, s8
	s_addc_u32 s4, s13, s9
	s_lshl_b32 s2, s6, 1
	s_and_b32 s8, s2, 0x380
	s_and_b32 s2, s7, 0x7e0
	s_and_b32 s7, s7, 0xe0
	s_cmpk_lt_u32 s7, 0x80
	s_cselect_b64 vcc, -1, 0
	s_lshl_b32 s6, s6, 4
	v_or_b32_e32 v4, s7, v7
	s_and_b32 s6, s6, 0x380
	v_or_b32_e32 v40, s6, v4
	s_addk_i32 s6, 0x380
	v_add_u32_e32 v4, s6, v4
	v_cndmask_b32_e32 v4, v4, v40, vcc
	v_or_b32_e32 v42, s8, v1
	v_lshlrev_b32_e32 v4, 2, v4
	v_lshl_add_u64 v[40:41], s[46:47], 0, v[4:5]
	v_lshlrev_b32_e32 v4, 13, v42
	v_lshl_add_u64 v[96:97], v[40:41], 0, v[4:5]
	v_add_co_u32_e32 v44, vcc, s19, v96
	global_load_dwordx4 v[40:43], v[96:97], off nt
	s_nop 0
	v_addc_co_u32_e32 v45, vcc, 0, v97, vcc
	global_load_dwordx4 v[44:47], v[44:45], off nt
	v_add_co_u32_e32 v48, vcc, s21, v96
	s_add_u32 s6, s5, s8
	s_nop 0
	v_addc_co_u32_e32 v49, vcc, 0, v97, vcc
	v_add_co_u32_e32 v52, vcc, s23, v96
	global_load_dwordx4 v[48:51], v[48:49], off nt
	s_nop 0
	v_addc_co_u32_e32 v53, vcc, 0, v97, vcc
	global_load_dwordx4 v[52:55], v[52:53], off nt
	v_add_co_u32_e32 v56, vcc, s25, v96
	s_addc_u32 s7, s4, 0
	s_nop 0
	v_addc_co_u32_e32 v57, vcc, 0, v97, vcc
	v_add_co_u32_e32 v60, vcc, s27, v96
	global_load_dwordx4 v[56:59], v[56:57], off nt
	s_nop 0
	v_addc_co_u32_e32 v61, vcc, 0, v97, vcc
	global_load_dwordx4 v[60:63], v[60:61], off nt
	v_add_co_u32_e32 v64, vcc, s29, v96
	v_readlane_b32 s61, v255, 4
	s_nop 0
	v_addc_co_u32_e32 v65, vcc, 0, v97, vcc
	v_add_co_u32_e32 v68, vcc, s31, v96
	global_load_dwordx4 v[64:67], v[64:65], off nt
	s_nop 0
	v_addc_co_u32_e32 v69, vcc, 0, v97, vcc
	global_load_dwordx4 v[68:71], v[68:69], off nt
	v_add_co_u32_e32 v72, vcc, s35, v96
	v_readlane_b32 s62, v255, 5
	s_nop 0
	v_addc_co_u32_e32 v73, vcc, 0, v97, vcc
	v_add_co_u32_e32 v76, vcc, s38, v96
	v_readlane_b32 s63, v255, 6
	s_nop 0
	v_addc_co_u32_e32 v77, vcc, 0, v97, vcc
	global_load_dwordx4 v[72:75], v[72:73], off nt
	s_nop 0
	global_load_dwordx4 v[76:79], v[76:77], off nt
	v_add_co_u32_e32 v80, vcc, s39, v96
	v_readlane_b32 s64, v255, 7
	s_nop 0
	v_addc_co_u32_e32 v81, vcc, 0, v97, vcc
	v_add_co_u32_e32 v84, vcc, s40, v96
	v_readlane_b32 s65, v255, 8
	s_nop 0
	v_addc_co_u32_e32 v85, vcc, 0, v97, vcc
	global_load_dwordx4 v[80:83], v[80:81], off nt
	s_nop 0
	global_load_dwordx4 v[84:87], v[84:85], off nt
	v_add_co_u32_e32 v88, vcc, s41, v96
	v_readlane_b32 s66, v255, 9
	s_nop 0
	v_addc_co_u32_e32 v89, vcc, 0, v97, vcc
	v_add_co_u32_e32 v92, vcc, s42, v96
	v_readlane_b32 s67, v255, 10
	s_nop 0
	v_addc_co_u32_e32 v93, vcc, 0, v97, vcc
	global_load_dwordx4 v[88:91], v[88:89], off nt
	s_nop 0
	global_load_dwordx4 v[92:95], v[92:93], off nt
	v_add_co_u32_e32 v98, vcc, s43, v96
	v_readlane_b32 s68, v255, 11
	s_nop 0
	v_addc_co_u32_e32 v99, vcc, 0, v97, vcc
	v_add_co_u32_e32 v100, vcc, s44, v96
	v_readlane_b32 s69, v255, 12
	s_nop 0
	v_addc_co_u32_e32 v101, vcc, 0, v97, vcc
	global_load_dwordx4 v[96:99], v[98:99], off nt
	s_nop 0
	global_load_dwordx4 v[100:103], v[100:101], off nt
	s_waitcnt vmcnt(15)
	v_mul_f32_e32 v4, 0x42800000, v40
	v_mul_f32_e32 v40, 0x42800000, v41
	v_mul_f32_e32 v41, 0x42800000, v42
	v_mul_f32_e32 v42, 0x42800000, v43
	s_waitcnt vmcnt(14)
	v_mul_f32_e32 v43, 0x42800000, v44
	ds_write2_b32 v8, v4, v43 offset1:8
	v_mul_f32_e32 v4, 0x42800000, v45
	ds_write2_b32 v8, v40, v4 offset0:129 offset1:137
	v_mul_f32_e32 v4, 0x42800000, v46
	ds_write2_b32 v38, v41, v4 offset0:2 offset1:10
	v_mul_f32_e32 v4, 0x42800000, v47
	ds_write2_b32 v38, v42, v4 offset0:131 offset1:139
	s_waitcnt vmcnt(13)
	v_mul_f32_e32 v4, 0x42800000, v48
	s_waitcnt vmcnt(12)
	v_mul_f32_e32 v43, 0x42800000, v52
	v_mul_f32_e32 v40, 0x42800000, v49
	ds_write2_b32 v8, v4, v43 offset0:16 offset1:24
	v_mul_f32_e32 v4, 0x42800000, v53
	v_mul_f32_e32 v41, 0x42800000, v50
	ds_write2_b32 v8, v40, v4 offset0:145 offset1:153
	v_mul_f32_e32 v4, 0x42800000, v54
	v_mul_f32_e32 v42, 0x42800000, v51
	ds_write2_b32 v38, v41, v4 offset0:18 offset1:26
	v_mul_f32_e32 v4, 0x42800000, v55
	ds_write2_b32 v38, v42, v4 offset0:147 offset1:155
	s_waitcnt vmcnt(11)
	v_mul_f32_e32 v4, 0x42800000, v56
	s_waitcnt vmcnt(10)
	v_mul_f32_e32 v43, 0x42800000, v60
	v_mul_f32_e32 v40, 0x42800000, v57
	ds_write2_b32 v8, v4, v43 offset0:32 offset1:40
	v_mul_f32_e32 v4, 0x42800000, v61
	v_mul_f32_e32 v41, 0x42800000, v58
	ds_write2_b32 v8, v40, v4 offset0:161 offset1:169
	v_mul_f32_e32 v4, 0x42800000, v62
	v_mul_f32_e32 v42, 0x42800000, v59
	ds_write2_b32 v38, v41, v4 offset0:34 offset1:42
	v_mul_f32_e32 v4, 0x42800000, v63
	ds_write2_b32 v38, v42, v4 offset0:163 offset1:171
	s_waitcnt vmcnt(9)
	v_mul_f32_e32 v4, 0x42800000, v64
	s_waitcnt vmcnt(8)
	v_mul_f32_e32 v43, 0x42800000, v68
	v_mul_f32_e32 v40, 0x42800000, v65
	ds_write2_b32 v8, v4, v43 offset0:48 offset1:56
	v_mul_f32_e32 v4, 0x42800000, v69
	v_mul_f32_e32 v41, 0x42800000, v66
	ds_write2_b32 v8, v40, v4 offset0:177 offset1:185
	v_mul_f32_e32 v4, 0x42800000, v70
	v_mul_f32_e32 v42, 0x42800000, v67
	ds_write2_b32 v38, v41, v4 offset0:50 offset1:58
	v_mul_f32_e32 v4, 0x42800000, v71
	ds_write2_b32 v38, v42, v4 offset0:179 offset1:187
	s_waitcnt vmcnt(7)
	v_mul_f32_e32 v4, 0x42800000, v72
	s_waitcnt vmcnt(6)
	v_mul_f32_e32 v43, 0x42800000, v76
	v_mul_f32_e32 v40, 0x42800000, v73
	ds_write2_b32 v8, v4, v43 offset0:64 offset1:72
	v_mul_f32_e32 v4, 0x42800000, v77
	v_mul_f32_e32 v41, 0x42800000, v74
	ds_write2_b32 v8, v40, v4 offset0:193 offset1:201
	v_mul_f32_e32 v4, 0x42800000, v78
	v_mul_f32_e32 v42, 0x42800000, v75
	ds_write2_b32 v38, v41, v4 offset0:66 offset1:74
	v_mul_f32_e32 v4, 0x42800000, v79
	ds_write2_b32 v38, v42, v4 offset0:195 offset1:203
	s_waitcnt vmcnt(5)
	v_mul_f32_e32 v4, 0x42800000, v80
	s_waitcnt vmcnt(4)
	v_mul_f32_e32 v43, 0x42800000, v84
	v_mul_f32_e32 v40, 0x42800000, v81
	ds_write2_b32 v8, v4, v43 offset0:80 offset1:88
	v_mul_f32_e32 v4, 0x42800000, v85
	v_mul_f32_e32 v41, 0x42800000, v82
	ds_write2_b32 v8, v40, v4 offset0:209 offset1:217
	v_mul_f32_e32 v4, 0x42800000, v86
	v_mul_f32_e32 v42, 0x42800000, v83
	ds_write2_b32 v38, v41, v4 offset0:82 offset1:90
	v_mul_f32_e32 v4, 0x42800000, v87
	ds_write2_b32 v38, v42, v4 offset0:211 offset1:219
	s_waitcnt vmcnt(3)
	v_mul_f32_e32 v4, 0x42800000, v88
	s_waitcnt vmcnt(2)
	v_mul_f32_e32 v43, 0x42800000, v92
	v_mul_f32_e32 v40, 0x42800000, v89
	ds_write2_b32 v8, v4, v43 offset0:96 offset1:104
	v_mul_f32_e32 v4, 0x42800000, v93
	v_mul_f32_e32 v41, 0x42800000, v90
	ds_write2_b32 v8, v40, v4 offset0:225 offset1:233
	v_mul_f32_e32 v4, 0x42800000, v94
	v_mul_f32_e32 v42, 0x42800000, v91
	ds_write2_b32 v38, v41, v4 offset0:98 offset1:106
	v_mul_f32_e32 v4, 0x42800000, v95
	ds_write2_b32 v38, v42, v4 offset0:227 offset1:235
	s_waitcnt vmcnt(1)
	v_mul_f32_e32 v4, 0x42800000, v96
	s_waitcnt vmcnt(0)
	v_mul_f32_e32 v43, 0x42800000, v100
	v_mul_f32_e32 v40, 0x42800000, v97
	ds_write2_b32 v8, v4, v43 offset0:112 offset1:120
	v_mul_f32_e32 v4, 0x42800000, v101
	v_mul_f32_e32 v41, 0x42800000, v98
	ds_write2_b32 v8, v40, v4 offset0:241 offset1:249
	v_mul_f32_e32 v4, 0x42800000, v102
	v_mul_f32_e32 v42, 0x42800000, v99
	ds_write2_b32 v38, v41, v4 offset0:114 offset1:122
	v_mul_f32_e32 v4, 0x42800000, v103
	ds_write2_b32 v38, v42, v4 offset0:243 offset1:251
	s_waitcnt lgkmcnt(0)
	ds_read2_b32 v[40:41], v13 offset1:1
	ds_read2_b32 v[42:43], v13 offset0:2 offset1:3
	ds_read2_b32 v[44:45], v13 offset0:4 offset1:5
	ds_read2_b32 v[46:47], v13 offset0:6 offset1:7
	v_lshl_add_u64 v[48:49], s[6:7], 0, v[2:3]
	v_readlane_b32 s70, v255, 13
	v_readlane_b32 s71, v255, 14
	s_waitcnt lgkmcnt(3)
	v_med3_f32 v4, v40, s34, v39
	v_med3_f32 v41, v41, s34, v39
	v_mov_b32_e32 v40, v5
	v_cvt_pk_fp8_f32 v40, v4, v41
	s_waitcnt lgkmcnt(2)
	v_med3_f32 v4, v42, s34, v39
	v_med3_f32 v41, v43, s34, v39
	s_waitcnt lgkmcnt(1)
	v_med3_f32 v42, v45, s34, v39
	v_cvt_pk_fp8_f32 v40, v4, v41 op_sel:[0,0,1]
	v_med3_f32 v4, v44, s34, v39
	v_mov_b32_e32 v41, v5
	v_cvt_pk_fp8_f32 v41, v4, v42
	ds_read2_b32 v[42:43], v13 offset0:8 offset1:9
	s_waitcnt lgkmcnt(1)
	v_med3_f32 v4, v46, s34, v39
	v_med3_f32 v44, v47, s34, v39
	v_cvt_pk_fp8_f32 v41, v4, v44 op_sel:[0,0,1]
	ds_read2_b32 v[44:45], v13 offset0:10 offset1:11
	ds_read2_b32 v[46:47], v13 offset0:12 offset1:13
	ds_read2_b32 v[50:51], v13 offset0:14 offset1:15
	s_waitcnt lgkmcnt(3)
	v_med3_f32 v4, v42, s34, v39
	v_med3_f32 v43, v43, s34, v39
	v_mov_b32_e32 v42, v5
	v_cvt_pk_fp8_f32 v42, v4, v43
	s_waitcnt lgkmcnt(2)
	v_med3_f32 v4, v44, s34, v39
	v_med3_f32 v44, v45, s34, v39
	s_waitcnt lgkmcnt(1)
	v_med3_f32 v45, v46, s34, v39
	v_med3_f32 v46, v47, s34, v39
	v_mov_b32_e32 v43, v5
	v_cvt_pk_fp8_f32 v43, v45, v46
	v_cvt_pk_fp8_f32 v42, v4, v44 op_sel:[0,0,1]
	s_waitcnt lgkmcnt(0)
	v_med3_f32 v4, v50, s34, v39
	v_med3_f32 v44, v51, s34, v39
	v_cvt_pk_fp8_f32 v43, v4, v44 op_sel:[0,0,1]
	ds_read2_b32 v[44:45], v14 offset1:1
	v_or_b32_e32 v4, s2, v1
	v_lshlrev_b32_e32 v4, 10, v4
	v_lshl_add_u64 v[46:47], v[48:49], 0, v[4:5]
	ds_read2_b32 v[50:51], v15 offset1:1
	ds_read2_b32 v[52:53], v16 offset1:1
	ds_read2_b32 v[54:55], v17 offset1:1
	s_waitcnt lgkmcnt(3)
	v_med3_f32 v4, v44, s34, v39
	v_med3_f32 v45, v45, s34, v39
	v_mov_b32_e32 v44, v5
	v_cvt_pk_fp8_f32 v44, v4, v45
	global_store_dwordx4 v[46:47], v[40:43], off nt
	s_waitcnt lgkmcnt(2)
	v_med3_f32 v4, v50, s34, v39
	v_mov_b32_e32 v45, v5
	v_med3_f32 v40, v51, s34, v39
	v_cvt_pk_fp8_f32 v44, v4, v40 op_sel:[0,0,1]
	s_waitcnt lgkmcnt(1)
	v_med3_f32 v4, v52, s34, v39
	v_med3_f32 v40, v53, s34, v39
	v_cvt_pk_fp8_f32 v45, v4, v40
	ds_read2_b32 v[40:41], v18 offset1:1
	s_waitcnt lgkmcnt(1)
	v_med3_f32 v4, v54, s34, v39
	v_med3_f32 v42, v55, s34, v39
	v_cvt_pk_fp8_f32 v45, v4, v42 op_sel:[0,0,1]
	ds_read2_b32 v[42:43], v19 offset1:1
	ds_read2_b32 v[50:51], v20 offset1:1
	ds_read2_b32 v[52:53], v21 offset1:1
	s_waitcnt lgkmcnt(3)
	v_med3_f32 v4, v40, s34, v39
	v_med3_f32 v40, v41, s34, v39
	v_mov_b32_e32 v46, v5
	v_cvt_pk_fp8_f32 v46, v4, v40
	s_waitcnt lgkmcnt(2)
	v_med3_f32 v4, v42, s34, v39
	s_waitcnt lgkmcnt(1)
	v_med3_f32 v41, v50, s34, v39
	v_med3_f32 v42, v51, s34, v39
	v_mov_b32_e32 v47, v5
	v_cvt_pk_fp8_f32 v47, v41, v42
	v_med3_f32 v40, v43, s34, v39
	v_cvt_pk_fp8_f32 v46, v4, v40 op_sel:[0,0,1]
	s_waitcnt lgkmcnt(0)
	v_med3_f32 v4, v52, s34, v39
	v_med3_f32 v40, v53, s34, v39
	v_cvt_pk_fp8_f32 v47, v4, v40 op_sel:[0,0,1]
	ds_read2_b32 v[40:41], v22 offset1:1
	v_or_b32_e32 v4, s2, v9
	v_lshlrev_b32_e32 v4, 10, v4
	v_lshl_add_u64 v[42:43], v[48:49], 0, v[4:5]
	ds_read2_b32 v[50:51], v23 offset1:1
	ds_read2_b32 v[52:53], v24 offset1:1
	ds_read2_b32 v[54:55], v25 offset1:1
	s_waitcnt lgkmcnt(3)
	v_med3_f32 v4, v40, s34, v39
	v_med3_f32 v41, v41, s34, v39
	v_mov_b32_e32 v40, v5
	v_cvt_pk_fp8_f32 v40, v4, v41
	s_waitcnt lgkmcnt(2)
	v_med3_f32 v4, v50, s34, v39
	v_med3_f32 v41, v51, s34, v39
	global_store_dwordx4 v[42:43], v[44:47], off nt
	v_cvt_pk_fp8_f32 v40, v4, v41 op_sel:[0,0,1]
	s_waitcnt lgkmcnt(1)
	v_med3_f32 v4, v52, s34, v39
	v_med3_f32 v42, v53, s34, v39
	v_mov_b32_e32 v41, v5
	v_cvt_pk_fp8_f32 v41, v4, v42
	ds_read2_b32 v[42:43], v26 offset1:1
	s_waitcnt lgkmcnt(1)
	v_med3_f32 v4, v54, s34, v39
	v_med3_f32 v44, v55, s34, v39
	v_cvt_pk_fp8_f32 v41, v4, v44 op_sel:[0,0,1]
	ds_read2_b32 v[44:45], v27 offset1:1
	ds_read2_b32 v[46:47], v28 offset1:1
	ds_read2_b32 v[50:51], v29 offset1:1
	s_waitcnt lgkmcnt(3)
	v_med3_f32 v4, v42, s34, v39
	v_med3_f32 v43, v43, s34, v39
	v_mov_b32_e32 v42, v5
	v_cvt_pk_fp8_f32 v42, v4, v43
	s_waitcnt lgkmcnt(2)
	v_med3_f32 v4, v44, s34, v39
	v_med3_f32 v44, v45, s34, v39
	s_waitcnt lgkmcnt(1)
	v_med3_f32 v45, v46, s34, v39
	v_med3_f32 v46, v47, s34, v39
	v_mov_b32_e32 v43, v5
	v_cvt_pk_fp8_f32 v43, v45, v46
	v_cvt_pk_fp8_f32 v42, v4, v44 op_sel:[0,0,1]
	s_waitcnt lgkmcnt(0)
	v_med3_f32 v4, v50, s34, v39
	v_med3_f32 v44, v51, s34, v39
	v_cvt_pk_fp8_f32 v43, v4, v44 op_sel:[0,0,1]
	ds_read2_b32 v[44:45], v30 offset1:1
	v_or_b32_e32 v4, s2, v10
	v_lshlrev_b32_e32 v4, 10, v4
	v_lshl_add_u64 v[46:47], v[48:49], 0, v[4:5]
	ds_read2_b32 v[50:51], v31 offset1:1
	ds_read2_b32 v[52:53], v32 offset1:1
	ds_read2_b32 v[54:55], v33 offset1:1
	s_waitcnt lgkmcnt(3)
	v_med3_f32 v4, v44, s34, v39
	v_med3_f32 v45, v45, s34, v39
	v_mov_b32_e32 v44, v5
	v_cvt_pk_fp8_f32 v44, v4, v45
	global_store_dwordx4 v[46:47], v[40:43], off nt
	s_waitcnt lgkmcnt(2)
	v_med3_f32 v4, v50, s34, v39
	v_mov_b32_e32 v45, v5
	v_med3_f32 v40, v51, s34, v39
	v_cvt_pk_fp8_f32 v44, v4, v40 op_sel:[0,0,1]
	s_waitcnt lgkmcnt(1)
	v_med3_f32 v4, v52, s34, v39
	v_med3_f32 v40, v53, s34, v39
	v_cvt_pk_fp8_f32 v45, v4, v40
	ds_read2_b32 v[40:41], v34 offset1:1
	s_waitcnt lgkmcnt(1)
	v_med3_f32 v4, v54, s34, v39
	v_med3_f32 v42, v55, s34, v39
	v_cvt_pk_fp8_f32 v45, v4, v42 op_sel:[0,0,1]
	ds_read2_b32 v[42:43], v35 offset1:1
	ds_read2_b32 v[50:51], v36 offset1:1
	ds_read2_b32 v[52:53], v37 offset1:1
	s_waitcnt lgkmcnt(3)
	v_med3_f32 v4, v40, s34, v39
	v_med3_f32 v40, v41, s34, v39
	v_mov_b32_e32 v46, v5
	v_cvt_pk_fp8_f32 v46, v4, v40
	s_waitcnt lgkmcnt(2)
	v_med3_f32 v4, v42, s34, v39
	s_waitcnt lgkmcnt(1)
	v_med3_f32 v41, v50, s34, v39
	v_med3_f32 v42, v51, s34, v39
	v_mov_b32_e32 v47, v5
	v_cvt_pk_fp8_f32 v47, v41, v42
	v_med3_f32 v40, v43, s34, v39
	v_cvt_pk_fp8_f32 v46, v4, v40 op_sel:[0,0,1]
	s_waitcnt lgkmcnt(0)
	v_med3_f32 v4, v52, s34, v39
	v_med3_f32 v40, v53, s34, v39
	v_cvt_pk_fp8_f32 v47, v4, v40 op_sel:[0,0,1]
	v_or_b32_e32 v4, s2, v11
	v_lshlrev_b32_e32 v4, 10, v4
	v_lshl_add_u64 v[40:41], v[48:49], 0, v[4:5]
	global_store_dwordx4 v[40:41], v[44:47], off nt
	s_waitcnt lgkmcnt(0)
	s_mov_b64 s[54:55], s[74:75]
	s_branch .LBB0_619

.LBB0_693:
	s_or_b64 exec, exec, s[4:5]
	s_waitcnt lgkmcnt(0)
	s_barrier
	ds_read_b32 v4, v11
	s_mov_b64 s[4:5], -1
	s_waitcnt lgkmcnt(0)
	v_cmp_lt_u32_e32 vcc, s15, v4
	v_readfirstlane_b32 s2, v4
	s_cbranch_vccnz .LBB0_688
	s_lshl_b32 s6, s2, 3
	s_add_i32 s6, s6, s91
	s_cmpk_gt_u32 s6, 0x5fff
	s_cbranch_scc1 .LBB0_687
	s_lshl_b32 s7, s6, 5
	s_cmpk_gt_u32 s6, 0x3fff
	s_cbranch_scc0 .LBB0_697
	s_add_i32 s2, s6, 0xffffc000
	s_lshr_b32 s2, s2, 8
	s_lshl_b64 s[4:5], s[2:3], 20
	s_lshl_b64 s[8:9], s[2:3], 22
	s_add_u32 s8, s76, s8
	s_addc_u32 s9, s77, s9
	s_add_u32 s4, s10, s4
	s_addc_u32 s5, s11, s5
	s_lshl_b32 s2, s6, 2
	s_and_b32 s43, s2, 0x380
	s_and_b32 s2, s7, 0x3e0
	v_or_b32_e32 v4, s2, v6
	v_or_b32_e32 v39, s43, v1
	v_lshlrev_b32_e32 v4, 2, v4
	v_lshl_add_u64 v[40:41], s[8:9], 0, v[4:5]
	v_lshlrev_b32_e32 v4, 12, v39
	v_lshl_add_u64 v[96:97], v[40:41], 0, v[4:5]
	v_add_co_u32_e32 v44, vcc, s16, v96
	global_load_dwordx4 v[40:43], v[96:97], off nt
	s_nop 0
	v_addc_co_u32_e32 v45, vcc, 0, v97, vcc
	global_load_dwordx4 v[44:47], v[44:45], off nt
	v_add_co_u32_e32 v48, vcc, s17, v96
	s_add_u32 s4, s4, s43
	s_nop 0
	v_addc_co_u32_e32 v49, vcc, 0, v97, vcc
	v_add_co_u32_e32 v52, vcc, s18, v96
	global_load_dwordx4 v[48:51], v[48:49], off nt
	s_nop 0
	v_addc_co_u32_e32 v53, vcc, 0, v97, vcc
	global_load_dwordx4 v[52:55], v[52:53], off nt
	v_add_co_u32_e32 v56, vcc, s19, v96
	s_addc_u32 s5, s5, 0
	s_nop 0
	v_addc_co_u32_e32 v57, vcc, 0, v97, vcc
	v_add_co_u32_e32 v60, vcc, s20, v96
	global_load_dwordx4 v[56:59], v[56:57], off nt
	s_nop 0
	v_addc_co_u32_e32 v61, vcc, 0, v97, vcc
	global_load_dwordx4 v[60:63], v[60:61], off nt
	v_add_co_u32_e32 v64, vcc, s21, v96
	s_nop 1
	v_addc_co_u32_e32 v65, vcc, 0, v97, vcc
	v_add_co_u32_e32 v68, vcc, s22, v96
	global_load_dwordx4 v[64:67], v[64:65], off nt
	s_nop 0
	v_addc_co_u32_e32 v69, vcc, 0, v97, vcc
	global_load_dwordx4 v[68:71], v[68:69], off nt
	v_add_co_u32_e32 v72, vcc, s23, v96
	s_waitcnt vmcnt(7)
	v_mul_f32_e32 v4, 0x42800000, v40
	v_addc_co_u32_e32 v73, vcc, 0, v97, vcc
	v_add_co_u32_e32 v76, vcc, s24, v96
	v_mul_f32_e32 v40, 0x42800000, v42
	s_nop 0
	v_addc_co_u32_e32 v77, vcc, 0, v97, vcc
	global_load_dwordx4 v[72:75], v[72:73], off nt
	s_nop 0
	global_load_dwordx4 v[76:79], v[76:77], off nt
	v_add_co_u32_e32 v80, vcc, s25, v96
	s_waitcnt vmcnt(8)
	v_mul_f32_e32 v42, 0x42800000, v44
	v_addc_co_u32_e32 v81, vcc, 0, v97, vcc
	v_add_co_u32_e32 v84, vcc, s26, v96
	v_mul_f32_e32 v39, 0x42800000, v41
	s_nop 0
	v_addc_co_u32_e32 v85, vcc, 0, v97, vcc
	global_load_dwordx4 v[80:83], v[80:81], off nt
	s_nop 0
	global_load_dwordx4 v[84:87], v[84:85], off nt
	v_add_co_u32_e32 v88, vcc, s27, v96
	v_mul_f32_e32 v41, 0x42800000, v43
	s_nop 0
	v_addc_co_u32_e32 v89, vcc, 0, v97, vcc
	v_add_co_u32_e32 v92, vcc, s28, v96
	s_nop 1
	v_addc_co_u32_e32 v93, vcc, 0, v97, vcc
	global_load_dwordx4 v[88:91], v[88:89], off nt
	s_nop 0
	global_load_dwordx4 v[92:95], v[92:93], off nt
	v_add_co_u32_e32 v98, vcc, s29, v96
	s_nop 1
	v_addc_co_u32_e32 v99, vcc, 0, v97, vcc
	v_add_co_u32_e32 v100, vcc, s30, v96
	s_nop 1
	v_addc_co_u32_e32 v101, vcc, 0, v97, vcc
	global_load_dwordx4 v[96:99], v[98:99], off nt
	s_nop 0
	global_load_dwordx4 v[100:103], v[100:101], off nt
	ds_write2_b32 v7, v4, v42 offset1:8
	v_mul_f32_e32 v4, 0x42800000, v45
	ds_write2_b32 v7, v39, v4 offset0:129 offset1:137
	v_mul_f32_e32 v4, 0x42800000, v46
	ds_write2_b32 v37, v40, v4 offset0:2 offset1:10
	v_mul_f32_e32 v4, 0x42800000, v47
	ds_write2_b32 v37, v41, v4 offset0:131 offset1:139
	s_waitcnt vmcnt(13)
	v_mul_f32_e32 v4, 0x42800000, v48
	s_waitcnt vmcnt(12)
	v_mul_f32_e32 v42, 0x42800000, v52
	v_mul_f32_e32 v39, 0x42800000, v49
	ds_write2_b32 v7, v4, v42 offset0:16 offset1:24
	v_mul_f32_e32 v4, 0x42800000, v53
	v_mul_f32_e32 v40, 0x42800000, v50
	ds_write2_b32 v7, v39, v4 offset0:145 offset1:153
	v_mul_f32_e32 v4, 0x42800000, v54
	v_mul_f32_e32 v41, 0x42800000, v51
	ds_write2_b32 v37, v40, v4 offset0:18 offset1:26
	v_mul_f32_e32 v4, 0x42800000, v55
	ds_write2_b32 v37, v41, v4 offset0:147 offset1:155
	s_waitcnt vmcnt(11)
	v_mul_f32_e32 v4, 0x42800000, v56
	s_waitcnt vmcnt(10)
	v_mul_f32_e32 v42, 0x42800000, v60
	v_mul_f32_e32 v39, 0x42800000, v57
	ds_write2_b32 v7, v4, v42 offset0:32 offset1:40
	v_mul_f32_e32 v4, 0x42800000, v61
	v_mul_f32_e32 v40, 0x42800000, v58
	ds_write2_b32 v7, v39, v4 offset0:161 offset1:169
	v_mul_f32_e32 v4, 0x42800000, v62
	v_mul_f32_e32 v41, 0x42800000, v59
	ds_write2_b32 v37, v40, v4 offset0:34 offset1:42
	v_mul_f32_e32 v4, 0x42800000, v63
	ds_write2_b32 v37, v41, v4 offset0:163 offset1:171
	s_waitcnt vmcnt(9)
	v_mul_f32_e32 v4, 0x42800000, v64
	s_waitcnt vmcnt(8)
	v_mul_f32_e32 v42, 0x42800000, v68
	v_mul_f32_e32 v39, 0x42800000, v65
	ds_write2_b32 v7, v4, v42 offset0:48 offset1:56
	v_mul_f32_e32 v4, 0x42800000, v69
	v_mul_f32_e32 v40, 0x42800000, v66
	ds_write2_b32 v7, v39, v4 offset0:177 offset1:185
	v_mul_f32_e32 v4, 0x42800000, v70
	v_mul_f32_e32 v41, 0x42800000, v67
	ds_write2_b32 v37, v40, v4 offset0:50 offset1:58
	v_mul_f32_e32 v4, 0x42800000, v71
	ds_write2_b32 v37, v41, v4 offset0:179 offset1:187
	v_lshl_add_u64 v[48:49], s[4:5], 0, v[2:3]
	s_mov_b64 s[4:5], 0
	s_waitcnt vmcnt(7)
	v_mul_f32_e32 v4, 0x42800000, v72
	s_waitcnt vmcnt(6)
	v_mul_f32_e32 v42, 0x42800000, v76
	v_mul_f32_e32 v39, 0x42800000, v73
	ds_write2_b32 v7, v4, v42 offset0:64 offset1:72
	v_mul_f32_e32 v4, 0x42800000, v77
	v_mul_f32_e32 v40, 0x42800000, v74
	ds_write2_b32 v7, v39, v4 offset0:193 offset1:201
	v_mul_f32_e32 v4, 0x42800000, v78
	v_mul_f32_e32 v41, 0x42800000, v75
	ds_write2_b32 v37, v40, v4 offset0:66 offset1:74
	v_mul_f32_e32 v4, 0x42800000, v79
	ds_write2_b32 v37, v41, v4 offset0:195 offset1:203
	s_waitcnt vmcnt(5)
	v_mul_f32_e32 v4, 0x42800000, v80
	s_waitcnt vmcnt(4)
	v_mul_f32_e32 v42, 0x42800000, v84
	v_mul_f32_e32 v39, 0x42800000, v81
	ds_write2_b32 v7, v4, v42 offset0:80 offset1:88
	v_mul_f32_e32 v4, 0x42800000, v85
	v_mul_f32_e32 v40, 0x42800000, v82
	ds_write2_b32 v7, v39, v4 offset0:209 offset1:217
	v_mul_f32_e32 v4, 0x42800000, v86
	v_mul_f32_e32 v41, 0x42800000, v83
	ds_write2_b32 v37, v40, v4 offset0:82 offset1:90
	v_mul_f32_e32 v4, 0x42800000, v87
	ds_write2_b32 v37, v41, v4 offset0:211 offset1:219
	s_waitcnt vmcnt(3)
	v_mul_f32_e32 v4, 0x42800000, v88
	s_waitcnt vmcnt(2)
	v_mul_f32_e32 v42, 0x42800000, v92
	v_mul_f32_e32 v39, 0x42800000, v89
	ds_write2_b32 v7, v4, v42 offset0:96 offset1:104
	v_mul_f32_e32 v4, 0x42800000, v93
	v_mul_f32_e32 v40, 0x42800000, v90
	ds_write2_b32 v7, v39, v4 offset0:225 offset1:233
	v_mul_f32_e32 v4, 0x42800000, v94
	v_mul_f32_e32 v41, 0x42800000, v91
	ds_write2_b32 v37, v40, v4 offset0:98 offset1:106
	v_mul_f32_e32 v4, 0x42800000, v95
	ds_write2_b32 v37, v41, v4 offset0:227 offset1:235
	s_waitcnt vmcnt(1)
	v_mul_f32_e32 v4, 0x42800000, v96
	s_waitcnt vmcnt(0)
	v_mul_f32_e32 v42, 0x42800000, v100
	v_mul_f32_e32 v39, 0x42800000, v97
	ds_write2_b32 v7, v4, v42 offset0:112 offset1:120
	v_mul_f32_e32 v4, 0x42800000, v101
	v_mul_f32_e32 v40, 0x42800000, v98
	ds_write2_b32 v7, v39, v4 offset0:241 offset1:249
	v_mul_f32_e32 v4, 0x42800000, v102
	v_mul_f32_e32 v41, 0x42800000, v99
	ds_write2_b32 v37, v40, v4 offset0:114 offset1:122
	v_mul_f32_e32 v4, 0x42800000, v103
	ds_write2_b32 v37, v41, v4 offset0:243 offset1:251
	s_waitcnt lgkmcnt(0)
	ds_read2_b32 v[40:41], v12 offset1:1
	ds_read2_b32 v[42:43], v12 offset0:2 offset1:3
	ds_read2_b32 v[44:45], v12 offset0:4 offset1:5
	ds_read2_b32 v[46:47], v12 offset0:6 offset1:7
	s_waitcnt lgkmcnt(3)
	v_med3_f32 v4, v40, s31, v38
	v_med3_f32 v39, v41, s31, v38
	v_mov_b32_e32 v40, v5
	v_cvt_pk_fp8_f32 v40, v4, v39
	s_waitcnt lgkmcnt(2)
	v_med3_f32 v4, v42, s31, v38
	v_med3_f32 v39, v43, s31, v38
	v_mov_b32_e32 v41, v5
	v_cvt_pk_fp8_f32 v40, v4, v39 op_sel:[0,0,1]
	s_waitcnt lgkmcnt(1)
	v_med3_f32 v4, v44, s31, v38
	v_med3_f32 v39, v45, s31, v38
	ds_read2_b32 v[42:43], v12 offset0:8 offset1:9
	v_cvt_pk_fp8_f32 v41, v4, v39
	s_waitcnt lgkmcnt(1)
	v_med3_f32 v4, v46, s31, v38
	v_med3_f32 v39, v47, s31, v38
	ds_read2_b32 v[44:45], v12 offset0:10 offset1:11
	ds_read2_b32 v[46:47], v12 offset0:12 offset1:13
	ds_read2_b32 v[50:51], v12 offset0:14 offset1:15
	v_cvt_pk_fp8_f32 v41, v4, v39 op_sel:[0,0,1]
	s_waitcnt lgkmcnt(3)
	v_med3_f32 v4, v42, s31, v38
	v_med3_f32 v39, v43, s31, v38
	v_mov_b32_e32 v42, v5
	v_cvt_pk_fp8_f32 v42, v4, v39
	s_waitcnt lgkmcnt(2)
	v_med3_f32 v4, v44, s31, v38
	v_med3_f32 v39, v45, s31, v38
	s_waitcnt lgkmcnt(1)
	v_med3_f32 v44, v46, s31, v38
	v_med3_f32 v45, v47, s31, v38
	v_mov_b32_e32 v43, v5
	v_cvt_pk_fp8_f32 v43, v44, v45
	ds_read2_b32 v[44:45], v13 offset1:1
	v_cvt_pk_fp8_f32 v42, v4, v39 op_sel:[0,0,1]
	s_waitcnt lgkmcnt(1)
	v_med3_f32 v4, v50, s31, v38
	v_med3_f32 v39, v51, s31, v38
	v_cvt_pk_fp8_f32 v43, v4, v39 op_sel:[0,0,1]
	v_or_b32_e32 v4, s2, v1
	v_lshlrev_b32_e32 v4, 10, v4
	v_lshl_add_u64 v[46:47], v[48:49], 0, v[4:5]
	s_waitcnt lgkmcnt(0)
	v_med3_f32 v4, v44, s31, v38
	v_med3_f32 v39, v45, s31, v38
	v_mov_b32_e32 v44, v5
	ds_read2_b32 v[50:51], v14 offset1:1
	ds_read2_b32 v[52:53], v15 offset1:1
	ds_read2_b32 v[54:55], v16 offset1:1
	v_cvt_pk_fp8_f32 v44, v4, v39
	global_store_dwordx4 v[46:47], v[40:43], off nt
	s_waitcnt lgkmcnt(2)
	v_med3_f32 v4, v50, s31, v38
	v_med3_f32 v39, v51, s31, v38
	v_cvt_pk_fp8_f32 v44, v4, v39 op_sel:[0,0,1]
	s_waitcnt lgkmcnt(1)
	v_med3_f32 v4, v52, s31, v38
	v_med3_f32 v39, v53, s31, v38
	v_mov_b32_e32 v45, v5
	ds_read2_b32 v[40:41], v17 offset1:1
	v_cvt_pk_fp8_f32 v45, v4, v39
	ds_read2_b32 v[42:43], v18 offset1:1
	ds_read2_b32 v[50:51], v19 offset1:1
	ds_read2_b32 v[52:53], v20 offset1:1
	s_waitcnt lgkmcnt(4)
	v_med3_f32 v4, v54, s31, v38
	v_med3_f32 v39, v55, s31, v38
	v_cvt_pk_fp8_f32 v45, v4, v39 op_sel:[0,0,1]
	s_waitcnt lgkmcnt(3)
	v_med3_f32 v4, v40, s31, v38
	v_med3_f32 v39, v41, s31, v38
	v_mov_b32_e32 v46, v5
	v_cvt_pk_fp8_f32 v46, v4, v39
	s_waitcnt lgkmcnt(1)
	v_med3_f32 v40, v50, s31, v38
	v_med3_f32 v41, v51, s31, v38
	v_mov_b32_e32 v47, v5
	v_cvt_pk_fp8_f32 v47, v40, v41
	ds_read2_b32 v[40:41], v21 offset1:1
	v_med3_f32 v4, v42, s31, v38
	v_med3_f32 v39, v43, s31, v38
	v_cvt_pk_fp8_f32 v46, v4, v39 op_sel:[0,0,1]
	s_waitcnt lgkmcnt(1)
	v_med3_f32 v4, v52, s31, v38
	v_med3_f32 v39, v53, s31, v38
	v_cvt_pk_fp8_f32 v47, v4, v39 op_sel:[0,0,1]
	v_or_b32_e32 v4, s2, v8
	v_lshlrev_b32_e32 v4, 10, v4
	v_lshl_add_u64 v[42:43], v[48:49], 0, v[4:5]
	s_waitcnt lgkmcnt(0)
	v_med3_f32 v4, v40, s31, v38
	v_med3_f32 v39, v41, s31, v38
	v_mov_b32_e32 v40, v5
	ds_read2_b32 v[50:51], v22 offset1:1
	ds_read2_b32 v[52:53], v23 offset1:1
	ds_read2_b32 v[54:55], v24 offset1:1
	v_cvt_pk_fp8_f32 v40, v4, v39
	global_store_dwordx4 v[42:43], v[44:47], off nt
	s_waitcnt lgkmcnt(2)
	v_med3_f32 v4, v50, s31, v38
	v_med3_f32 v39, v51, s31, v38
	v_cvt_pk_fp8_f32 v40, v4, v39 op_sel:[0,0,1]
	s_waitcnt lgkmcnt(1)
	v_med3_f32 v4, v52, s31, v38
	v_med3_f32 v39, v53, s31, v38
	v_mov_b32_e32 v41, v5
	ds_read2_b32 v[42:43], v25 offset1:1
	v_cvt_pk_fp8_f32 v41, v4, v39
	ds_read2_b32 v[44:45], v26 offset1:1
	ds_read2_b32 v[46:47], v27 offset1:1
	ds_read2_b32 v[50:51], v28 offset1:1
	s_waitcnt lgkmcnt(4)
	v_med3_f32 v4, v54, s31, v38
	v_med3_f32 v39, v55, s31, v38
	v_cvt_pk_fp8_f32 v41, v4, v39 op_sel:[0,0,1]
	s_waitcnt lgkmcnt(3)
	v_med3_f32 v4, v42, s31, v38
	v_med3_f32 v39, v43, s31, v38
	v_mov_b32_e32 v42, v5
	v_cvt_pk_fp8_f32 v42, v4, v39
	s_waitcnt lgkmcnt(2)
	v_med3_f32 v4, v44, s31, v38
	v_med3_f32 v39, v45, s31, v38
	s_waitcnt lgkmcnt(1)
	v_med3_f32 v44, v46, s31, v38
	v_med3_f32 v45, v47, s31, v38
	v_mov_b32_e32 v43, v5
	v_cvt_pk_fp8_f32 v43, v44, v45
	ds_read2_b32 v[44:45], v29 offset1:1
	v_cvt_pk_fp8_f32 v42, v4, v39 op_sel:[0,0,1]
	s_waitcnt lgkmcnt(1)
	v_med3_f32 v4, v50, s31, v38
	v_med3_f32 v39, v51, s31, v38
	v_cvt_pk_fp8_f32 v43, v4, v39 op_sel:[0,0,1]
	v_or_b32_e32 v4, s2, v9
	v_lshlrev_b32_e32 v4, 10, v4
	v_lshl_add_u64 v[46:47], v[48:49], 0, v[4:5]
	s_waitcnt lgkmcnt(0)
	v_med3_f32 v4, v44, s31, v38
	v_med3_f32 v39, v45, s31, v38
	v_mov_b32_e32 v44, v5
	ds_read2_b32 v[50:51], v30 offset1:1
	ds_read2_b32 v[52:53], v31 offset1:1
	ds_read2_b32 v[54:55], v32 offset1:1
	v_cvt_pk_fp8_f32 v44, v4, v39
	global_store_dwordx4 v[46:47], v[40:43], off nt
	s_waitcnt lgkmcnt(2)
	v_med3_f32 v4, v50, s31, v38
	v_med3_f32 v39, v51, s31, v38
	v_cvt_pk_fp8_f32 v44, v4, v39 op_sel:[0,0,1]
	s_waitcnt lgkmcnt(1)
	v_med3_f32 v4, v52, s31, v38
	v_med3_f32 v39, v53, s31, v38
	v_mov_b32_e32 v45, v5
	ds_read2_b32 v[40:41], v33 offset1:1
	v_cvt_pk_fp8_f32 v45, v4, v39
	ds_read2_b32 v[42:43], v34 offset1:1
	ds_read2_b32 v[50:51], v35 offset1:1
	ds_read2_b32 v[52:53], v36 offset1:1
	s_waitcnt lgkmcnt(4)
	v_med3_f32 v4, v54, s31, v38
	v_med3_f32 v39, v55, s31, v38
	v_cvt_pk_fp8_f32 v45, v4, v39 op_sel:[0,0,1]
	s_waitcnt lgkmcnt(3)
	v_med3_f32 v4, v40, s31, v38
	v_med3_f32 v39, v41, s31, v38
	v_mov_b32_e32 v46, v5
	v_cvt_pk_fp8_f32 v46, v4, v39
	s_waitcnt lgkmcnt(1)
	v_med3_f32 v40, v50, s31, v38
	v_med3_f32 v41, v51, s31, v38
	v_mov_b32_e32 v47, v5
	v_cvt_pk_fp8_f32 v47, v40, v41
	v_med3_f32 v4, v42, s31, v38
	v_med3_f32 v39, v43, s31, v38
	v_cvt_pk_fp8_f32 v46, v4, v39 op_sel:[0,0,1]
	s_waitcnt lgkmcnt(0)
	v_med3_f32 v4, v52, s31, v38
	v_med3_f32 v39, v53, s31, v38
	v_cvt_pk_fp8_f32 v47, v4, v39 op_sel:[0,0,1]
	v_or_b32_e32 v4, s2, v10
	v_lshlrev_b32_e32 v4, 10, v4
	v_lshl_add_u64 v[40:41], v[48:49], 0, v[4:5]
	global_store_dwordx4 v[40:41], v[44:47], off nt
	s_waitcnt lgkmcnt(0)
.LBB0_697:
	s_andn2_b64 vcc, exec, s[4:5]
	s_cbranch_vccnz .LBB0_687
	v_readlane_b32 s60, v255, 3
	s_lshr_b32 s2, s6, 9
	v_readlane_b32 s72, v255, 15
	v_readlane_b32 s73, v255, 16
	s_lshl_b64 s[4:5], s[2:3], 23
	v_readlane_b32 s74, v255, 17
	v_readlane_b32 s75, v255, 18
	s_mov_b64 s[52:53], s[72:73]
	s_add_u32 s44, s52, s4
	s_addc_u32 s45, s53, s5
	s_lshl_b64 s[8:9], s[2:3], 21
	s_add_u32 s5, s12, s8
	s_addc_u32 s4, s13, s9
	s_lshl_b32 s2, s6, 1
	s_and_b32 s8, s2, 0x380
	s_and_b32 s2, s7, 0x7e0
	s_and_b32 s7, s7, 0xe0
	s_cmpk_lt_u32 s7, 0x80
	s_cselect_b64 vcc, -1, 0
	s_lshl_b32 s6, s6, 4
	v_or_b32_e32 v4, s7, v6
	s_and_b32 s6, s6, 0x380
	v_or_b32_e32 v39, s6, v4
	s_addk_i32 s6, 0x380
	v_add_u32_e32 v4, s6, v4
	v_cndmask_b32_e32 v4, v4, v39, vcc
	v_or_b32_e32 v39, s8, v1
	v_lshlrev_b32_e32 v4, 2, v4
	v_lshl_add_u64 v[40:41], s[44:45], 0, v[4:5]
	v_lshlrev_b32_e32 v4, 13, v39
	v_lshl_add_u64 v[96:97], v[40:41], 0, v[4:5]
	v_add_co_u32_e32 v44, vcc, s17, v96
	global_load_dwordx4 v[40:43], v[96:97], off nt
	s_nop 0
	v_addc_co_u32_e32 v45, vcc, 0, v97, vcc
	global_load_dwordx4 v[44:47], v[44:45], off nt
	v_add_co_u32_e32 v48, vcc, s19, v96
	s_add_u32 s6, s5, s8
	s_nop 0
	v_addc_co_u32_e32 v49, vcc, 0, v97, vcc
	v_add_co_u32_e32 v52, vcc, s21, v96
	global_load_dwordx4 v[48:51], v[48:49], off nt
	s_nop 0
	v_addc_co_u32_e32 v53, vcc, 0, v97, vcc
	global_load_dwordx4 v[52:55], v[52:53], off nt
	v_add_co_u32_e32 v56, vcc, s23, v96
	s_addc_u32 s7, s4, 0
	s_nop 0
	v_addc_co_u32_e32 v57, vcc, 0, v97, vcc
	v_add_co_u32_e32 v60, vcc, s25, v96
	global_load_dwordx4 v[56:59], v[56:57], off nt
	s_nop 0
	v_addc_co_u32_e32 v61, vcc, 0, v97, vcc
	global_load_dwordx4 v[60:63], v[60:61], off nt
	v_add_co_u32_e32 v64, vcc, s27, v96
	v_readlane_b32 s61, v255, 4
	s_nop 0
	v_addc_co_u32_e32 v65, vcc, 0, v97, vcc
	v_add_co_u32_e32 v68, vcc, s29, v96
	global_load_dwordx4 v[64:67], v[64:65], off nt
	s_nop 0
	v_addc_co_u32_e32 v69, vcc, 0, v97, vcc
	global_load_dwordx4 v[68:71], v[68:69], off nt
	v_add_co_u32_e32 v72, vcc, s33, v96
	v_readlane_b32 s62, v255, 5
	s_nop 0
	v_addc_co_u32_e32 v73, vcc, 0, v97, vcc
	v_add_co_u32_e32 v76, vcc, s34, v96
	v_readlane_b32 s63, v255, 6
	s_nop 0
	v_addc_co_u32_e32 v77, vcc, 0, v97, vcc
	global_load_dwordx4 v[72:75], v[72:73], off nt
	s_nop 0
	global_load_dwordx4 v[76:79], v[76:77], off nt
	v_add_co_u32_e32 v80, vcc, s35, v96
	v_readlane_b32 s64, v255, 7
	s_nop 0
	v_addc_co_u32_e32 v81, vcc, 0, v97, vcc
	v_add_co_u32_e32 v84, vcc, s38, v96
	v_readlane_b32 s65, v255, 8
	s_nop 0
	v_addc_co_u32_e32 v85, vcc, 0, v97, vcc
	global_load_dwordx4 v[80:83], v[80:81], off nt
	s_nop 0
	global_load_dwordx4 v[84:87], v[84:85], off nt
	v_add_co_u32_e32 v88, vcc, s39, v96
	v_readlane_b32 s66, v255, 9
	s_nop 0
	v_addc_co_u32_e32 v89, vcc, 0, v97, vcc
	v_add_co_u32_e32 v92, vcc, s40, v96
	v_readlane_b32 s67, v255, 10
	s_nop 0
	v_addc_co_u32_e32 v93, vcc, 0, v97, vcc
	global_load_dwordx4 v[88:91], v[88:89], off nt
	s_nop 0
	global_load_dwordx4 v[92:95], v[92:93], off nt
	v_add_co_u32_e32 v98, vcc, s41, v96
	v_readlane_b32 s68, v255, 11
	s_nop 0
	v_addc_co_u32_e32 v99, vcc, 0, v97, vcc
	v_add_co_u32_e32 v100, vcc, s42, v96
	v_readlane_b32 s69, v255, 12
	s_nop 0
	v_addc_co_u32_e32 v101, vcc, 0, v97, vcc
	global_load_dwordx4 v[96:99], v[98:99], off nt
	s_nop 0
	global_load_dwordx4 v[100:103], v[100:101], off nt
	s_waitcnt vmcnt(15)
	v_mul_f32_e32 v4, 0x42800000, v40
	v_mul_f32_e32 v40, 0x42800000, v42
	s_waitcnt vmcnt(14)
	v_mul_f32_e32 v42, 0x42800000, v44
	v_mul_f32_e32 v39, 0x42800000, v41
	ds_write2_b32 v7, v4, v42 offset1:8
	v_mul_f32_e32 v4, 0x42800000, v45
	ds_write2_b32 v7, v39, v4 offset0:129 offset1:137
	v_mul_f32_e32 v4, 0x42800000, v46
	v_mul_f32_e32 v41, 0x42800000, v43
	ds_write2_b32 v37, v40, v4 offset0:2 offset1:10
	v_mul_f32_e32 v4, 0x42800000, v47
	ds_write2_b32 v37, v41, v4 offset0:131 offset1:139
	s_waitcnt vmcnt(13)
	v_mul_f32_e32 v4, 0x42800000, v48
	s_waitcnt vmcnt(12)
	v_mul_f32_e32 v42, 0x42800000, v52
	v_mul_f32_e32 v39, 0x42800000, v49
	ds_write2_b32 v7, v4, v42 offset0:16 offset1:24
	v_mul_f32_e32 v4, 0x42800000, v53
	v_mul_f32_e32 v40, 0x42800000, v50
	ds_write2_b32 v7, v39, v4 offset0:145 offset1:153
	v_mul_f32_e32 v4, 0x42800000, v54
	v_mul_f32_e32 v41, 0x42800000, v51
	ds_write2_b32 v37, v40, v4 offset0:18 offset1:26
	v_mul_f32_e32 v4, 0x42800000, v55
	ds_write2_b32 v37, v41, v4 offset0:147 offset1:155
	s_waitcnt vmcnt(11)
	v_mul_f32_e32 v4, 0x42800000, v56
	s_waitcnt vmcnt(10)
	v_mul_f32_e32 v42, 0x42800000, v60
	v_mul_f32_e32 v39, 0x42800000, v57
	ds_write2_b32 v7, v4, v42 offset0:32 offset1:40
	v_mul_f32_e32 v4, 0x42800000, v61
	v_mul_f32_e32 v40, 0x42800000, v58
	ds_write2_b32 v7, v39, v4 offset0:161 offset1:169
	v_mul_f32_e32 v4, 0x42800000, v62
	v_mul_f32_e32 v41, 0x42800000, v59
	ds_write2_b32 v37, v40, v4 offset0:34 offset1:42
	v_mul_f32_e32 v4, 0x42800000, v63
	ds_write2_b32 v37, v41, v4 offset0:163 offset1:171
	s_waitcnt vmcnt(9)
	v_mul_f32_e32 v4, 0x42800000, v64
	s_waitcnt vmcnt(8)
	v_mul_f32_e32 v42, 0x42800000, v68
	v_mul_f32_e32 v39, 0x42800000, v65
	ds_write2_b32 v7, v4, v42 offset0:48 offset1:56
	v_mul_f32_e32 v4, 0x42800000, v69
	v_mul_f32_e32 v40, 0x42800000, v66
	ds_write2_b32 v7, v39, v4 offset0:177 offset1:185
	v_mul_f32_e32 v4, 0x42800000, v70
	v_mul_f32_e32 v41, 0x42800000, v67
	ds_write2_b32 v37, v40, v4 offset0:50 offset1:58
	v_mul_f32_e32 v4, 0x42800000, v71
	ds_write2_b32 v37, v41, v4 offset0:179 offset1:187
	s_waitcnt vmcnt(7)
	v_mul_f32_e32 v4, 0x42800000, v72
	s_waitcnt vmcnt(6)
	v_mul_f32_e32 v42, 0x42800000, v76
	v_mul_f32_e32 v39, 0x42800000, v73
	ds_write2_b32 v7, v4, v42 offset0:64 offset1:72
	v_mul_f32_e32 v4, 0x42800000, v77
	v_mul_f32_e32 v40, 0x42800000, v74
	ds_write2_b32 v7, v39, v4 offset0:193 offset1:201
	v_mul_f32_e32 v4, 0x42800000, v78
	v_mul_f32_e32 v41, 0x42800000, v75
	ds_write2_b32 v37, v40, v4 offset0:66 offset1:74
	v_mul_f32_e32 v4, 0x42800000, v79
	ds_write2_b32 v37, v41, v4 offset0:195 offset1:203
	s_waitcnt vmcnt(5)
	v_mul_f32_e32 v4, 0x42800000, v80
	s_waitcnt vmcnt(4)
	v_mul_f32_e32 v42, 0x42800000, v84
	v_mul_f32_e32 v39, 0x42800000, v81
	ds_write2_b32 v7, v4, v42 offset0:80 offset1:88
	v_mul_f32_e32 v4, 0x42800000, v85
	v_mul_f32_e32 v40, 0x42800000, v82
	ds_write2_b32 v7, v39, v4 offset0:209 offset1:217
	v_mul_f32_e32 v4, 0x42800000, v86
	v_mul_f32_e32 v41, 0x42800000, v83
	ds_write2_b32 v37, v40, v4 offset0:82 offset1:90
	v_mul_f32_e32 v4, 0x42800000, v87
	ds_write2_b32 v37, v41, v4 offset0:211 offset1:219
	s_waitcnt vmcnt(3)
	v_mul_f32_e32 v4, 0x42800000, v88
	s_waitcnt vmcnt(2)
	v_mul_f32_e32 v42, 0x42800000, v92
	v_mul_f32_e32 v39, 0x42800000, v89
	ds_write2_b32 v7, v4, v42 offset0:96 offset1:104
	v_mul_f32_e32 v4, 0x42800000, v93
	v_mul_f32_e32 v40, 0x42800000, v90
	ds_write2_b32 v7, v39, v4 offset0:225 offset1:233
	v_mul_f32_e32 v4, 0x42800000, v94
	v_mul_f32_e32 v41, 0x42800000, v91
	ds_write2_b32 v37, v40, v4 offset0:98 offset1:106
	v_mul_f32_e32 v4, 0x42800000, v95
	ds_write2_b32 v37, v41, v4 offset0:227 offset1:235
	s_waitcnt vmcnt(1)
	v_mul_f32_e32 v4, 0x42800000, v96
	s_waitcnt vmcnt(0)
	v_mul_f32_e32 v42, 0x42800000, v100
	v_mul_f32_e32 v39, 0x42800000, v97
	ds_write2_b32 v7, v4, v42 offset0:112 offset1:120
	v_mul_f32_e32 v4, 0x42800000, v101
	v_mul_f32_e32 v40, 0x42800000, v98
	ds_write2_b32 v7, v39, v4 offset0:241 offset1:249
	v_mul_f32_e32 v4, 0x42800000, v102
	v_mul_f32_e32 v41, 0x42800000, v99
	ds_write2_b32 v37, v40, v4 offset0:114 offset1:122
	v_mul_f32_e32 v4, 0x42800000, v103
	ds_write2_b32 v37, v41, v4 offset0:243 offset1:251
	s_waitcnt lgkmcnt(0)
	ds_read2_b32 v[40:41], v12 offset1:1
	ds_read2_b32 v[42:43], v12 offset0:2 offset1:3
	ds_read2_b32 v[44:45], v12 offset0:4 offset1:5
	ds_read2_b32 v[46:47], v12 offset0:6 offset1:7
	v_lshl_add_u64 v[48:49], s[6:7], 0, v[2:3]
	v_readlane_b32 s70, v255, 13
	v_readlane_b32 s71, v255, 14
	s_waitcnt lgkmcnt(3)
	v_med3_f32 v4, v40, s31, v38
	v_med3_f32 v39, v41, s31, v38
	v_mov_b32_e32 v40, v5
	v_cvt_pk_fp8_f32 v40, v4, v39
	s_waitcnt lgkmcnt(2)
	v_med3_f32 v4, v42, s31, v38
	v_med3_f32 v39, v43, s31, v38
	v_mov_b32_e32 v41, v5
	v_cvt_pk_fp8_f32 v40, v4, v39 op_sel:[0,0,1]
	s_waitcnt lgkmcnt(1)
	v_med3_f32 v4, v44, s31, v38
	v_med3_f32 v39, v45, s31, v38
	ds_read2_b32 v[42:43], v12 offset0:8 offset1:9
	v_cvt_pk_fp8_f32 v41, v4, v39
	s_waitcnt lgkmcnt(1)
	v_med3_f32 v4, v46, s31, v38
	v_med3_f32 v39, v47, s31, v38
	ds_read2_b32 v[44:45], v12 offset0:10 offset1:11
	ds_read2_b32 v[46:47], v12 offset0:12 offset1:13
	ds_read2_b32 v[50:51], v12 offset0:14 offset1:15
	v_cvt_pk_fp8_f32 v41, v4, v39 op_sel:[0,0,1]
	s_waitcnt lgkmcnt(3)
	v_med3_f32 v4, v42, s31, v38
	v_med3_f32 v39, v43, s31, v38
	v_mov_b32_e32 v42, v5
	v_cvt_pk_fp8_f32 v42, v4, v39
	s_waitcnt lgkmcnt(2)
	v_med3_f32 v4, v44, s31, v38
	v_med3_f32 v39, v45, s31, v38
	s_waitcnt lgkmcnt(1)
	v_med3_f32 v44, v46, s31, v38
	v_med3_f32 v45, v47, s31, v38
	v_mov_b32_e32 v43, v5
	v_cvt_pk_fp8_f32 v43, v44, v45
	ds_read2_b32 v[44:45], v13 offset1:1
	v_cvt_pk_fp8_f32 v42, v4, v39 op_sel:[0,0,1]
	s_waitcnt lgkmcnt(1)
	v_med3_f32 v4, v50, s31, v38
	v_med3_f32 v39, v51, s31, v38
	v_cvt_pk_fp8_f32 v43, v4, v39 op_sel:[0,0,1]
	v_or_b32_e32 v4, s2, v1
	v_lshlrev_b32_e32 v4, 10, v4
	v_lshl_add_u64 v[46:47], v[48:49], 0, v[4:5]
	s_waitcnt lgkmcnt(0)
	v_med3_f32 v4, v44, s31, v38
	v_med3_f32 v39, v45, s31, v38
	v_mov_b32_e32 v44, v5
	ds_read2_b32 v[50:51], v14 offset1:1
	ds_read2_b32 v[52:53], v15 offset1:1
	ds_read2_b32 v[54:55], v16 offset1:1
	v_cvt_pk_fp8_f32 v44, v4, v39
	global_store_dwordx4 v[46:47], v[40:43], off nt
	s_waitcnt lgkmcnt(2)
	v_med3_f32 v4, v50, s31, v38
	v_med3_f32 v39, v51, s31, v38
	v_cvt_pk_fp8_f32 v44, v4, v39 op_sel:[0,0,1]
	s_waitcnt lgkmcnt(1)
	v_med3_f32 v4, v52, s31, v38
	v_med3_f32 v39, v53, s31, v38
	v_mov_b32_e32 v45, v5
	ds_read2_b32 v[40:41], v17 offset1:1
	v_cvt_pk_fp8_f32 v45, v4, v39
	ds_read2_b32 v[42:43], v18 offset1:1
	ds_read2_b32 v[50:51], v19 offset1:1
	ds_read2_b32 v[52:53], v20 offset1:1
	s_waitcnt lgkmcnt(4)
	v_med3_f32 v4, v54, s31, v38
	v_med3_f32 v39, v55, s31, v38
	v_cvt_pk_fp8_f32 v45, v4, v39 op_sel:[0,0,1]
	s_waitcnt lgkmcnt(3)
	v_med3_f32 v4, v40, s31, v38
	v_med3_f32 v39, v41, s31, v38
	v_mov_b32_e32 v46, v5
	v_cvt_pk_fp8_f32 v46, v4, v39
	s_waitcnt lgkmcnt(1)
	v_med3_f32 v40, v50, s31, v38
	v_med3_f32 v41, v51, s31, v38
	v_mov_b32_e32 v47, v5
	v_cvt_pk_fp8_f32 v47, v40, v41
	ds_read2_b32 v[40:41], v21 offset1:1
	v_med3_f32 v4, v42, s31, v38
	v_med3_f32 v39, v43, s31, v38
	v_cvt_pk_fp8_f32 v46, v4, v39 op_sel:[0,0,1]
	s_waitcnt lgkmcnt(1)
	v_med3_f32 v4, v52, s31, v38
	v_med3_f32 v39, v53, s31, v38
	v_cvt_pk_fp8_f32 v47, v4, v39 op_sel:[0,0,1]
	v_or_b32_e32 v4, s2, v8
	v_lshlrev_b32_e32 v4, 10, v4
	v_lshl_add_u64 v[42:43], v[48:49], 0, v[4:5]
	s_waitcnt lgkmcnt(0)
	v_med3_f32 v4, v40, s31, v38
	v_med3_f32 v39, v41, s31, v38
	v_mov_b32_e32 v40, v5
	ds_read2_b32 v[50:51], v22 offset1:1
	ds_read2_b32 v[52:53], v23 offset1:1
	ds_read2_b32 v[54:55], v24 offset1:1
	v_cvt_pk_fp8_f32 v40, v4, v39
	global_store_dwordx4 v[42:43], v[44:47], off nt
	s_waitcnt lgkmcnt(2)
	v_med3_f32 v4, v50, s31, v38
	v_med3_f32 v39, v51, s31, v38
	v_cvt_pk_fp8_f32 v40, v4, v39 op_sel:[0,0,1]
	s_waitcnt lgkmcnt(1)
	v_med3_f32 v4, v52, s31, v38
	v_med3_f32 v39, v53, s31, v38
	v_mov_b32_e32 v41, v5
	ds_read2_b32 v[42:43], v25 offset1:1
	v_cvt_pk_fp8_f32 v41, v4, v39
	ds_read2_b32 v[44:45], v26 offset1:1
	ds_read2_b32 v[46:47], v27 offset1:1
	ds_read2_b32 v[50:51], v28 offset1:1
	s_waitcnt lgkmcnt(4)
	v_med3_f32 v4, v54, s31, v38
	v_med3_f32 v39, v55, s31, v38
	v_cvt_pk_fp8_f32 v41, v4, v39 op_sel:[0,0,1]
	s_waitcnt lgkmcnt(3)
	v_med3_f32 v4, v42, s31, v38
	v_med3_f32 v39, v43, s31, v38
	v_mov_b32_e32 v42, v5
	v_cvt_pk_fp8_f32 v42, v4, v39
	s_waitcnt lgkmcnt(2)
	v_med3_f32 v4, v44, s31, v38
	v_med3_f32 v39, v45, s31, v38
	s_waitcnt lgkmcnt(1)
	v_med3_f32 v44, v46, s31, v38
	v_med3_f32 v45, v47, s31, v38
	v_mov_b32_e32 v43, v5
	v_cvt_pk_fp8_f32 v43, v44, v45
	ds_read2_b32 v[44:45], v29 offset1:1
	v_cvt_pk_fp8_f32 v42, v4, v39 op_sel:[0,0,1]
	s_waitcnt lgkmcnt(1)
	v_med3_f32 v4, v50, s31, v38
	v_med3_f32 v39, v51, s31, v38
	v_cvt_pk_fp8_f32 v43, v4, v39 op_sel:[0,0,1]
	v_or_b32_e32 v4, s2, v9
	v_lshlrev_b32_e32 v4, 10, v4
	v_lshl_add_u64 v[46:47], v[48:49], 0, v[4:5]
	s_waitcnt lgkmcnt(0)
	v_med3_f32 v4, v44, s31, v38
	v_med3_f32 v39, v45, s31, v38
	v_mov_b32_e32 v44, v5
	ds_read2_b32 v[50:51], v30 offset1:1
	ds_read2_b32 v[52:53], v31 offset1:1
	ds_read2_b32 v[54:55], v32 offset1:1
	v_cvt_pk_fp8_f32 v44, v4, v39
	global_store_dwordx4 v[46:47], v[40:43], off nt
	s_waitcnt lgkmcnt(2)
	v_med3_f32 v4, v50, s31, v38
	v_med3_f32 v39, v51, s31, v38
	v_cvt_pk_fp8_f32 v44, v4, v39 op_sel:[0,0,1]
	s_waitcnt lgkmcnt(1)
	v_med3_f32 v4, v52, s31, v38
	v_med3_f32 v39, v53, s31, v38
	v_mov_b32_e32 v45, v5
	ds_read2_b32 v[40:41], v33 offset1:1
	v_cvt_pk_fp8_f32 v45, v4, v39
	ds_read2_b32 v[42:43], v34 offset1:1
	ds_read2_b32 v[50:51], v35 offset1:1
	ds_read2_b32 v[52:53], v36 offset1:1
	s_waitcnt lgkmcnt(4)
	v_med3_f32 v4, v54, s31, v38
	v_med3_f32 v39, v55, s31, v38
	v_cvt_pk_fp8_f32 v45, v4, v39 op_sel:[0,0,1]
	s_waitcnt lgkmcnt(3)
	v_med3_f32 v4, v40, s31, v38
	v_med3_f32 v39, v41, s31, v38
	v_mov_b32_e32 v46, v5
	v_cvt_pk_fp8_f32 v46, v4, v39
	s_waitcnt lgkmcnt(1)
	v_med3_f32 v40, v50, s31, v38
	v_med3_f32 v41, v51, s31, v38
	v_mov_b32_e32 v47, v5
	v_cvt_pk_fp8_f32 v47, v40, v41
	v_med3_f32 v4, v42, s31, v38
	v_med3_f32 v39, v43, s31, v38
	v_cvt_pk_fp8_f32 v46, v4, v39 op_sel:[0,0,1]
	s_waitcnt lgkmcnt(0)
	v_med3_f32 v4, v52, s31, v38
	v_med3_f32 v39, v53, s31, v38
	v_cvt_pk_fp8_f32 v47, v4, v39 op_sel:[0,0,1]
	v_or_b32_e32 v4, s2, v10
	v_lshlrev_b32_e32 v4, 10, v4
	v_lshl_add_u64 v[40:41], v[48:49], 0, v[4:5]
	global_store_dwordx4 v[40:41], v[44:47], off nt
	s_waitcnt lgkmcnt(0)
	s_mov_b64 s[54:55], s[74:75]
	s_branch .LBB0_687
